# v17: v15 + P4 indexer loops: compare/select pairs on separate mask registers (hazard nops removed)
# baseline (speedup 1.0000x reference)
; __device__ __forceinline__ int crow(int reg, int h) { return (reg & 3) + 8 * (reg >> 2) + 4 * h; }
; __device__ __forceinline__ int bin2(float sv, int zi) {
;     const unsigned u = __float_as_uint(sv);
;     int c = (int)((u >> 20) & 0x7FFu) - 832;
;     c = c < 0 ? 0 : (c > 207 ? 207 : c);
;     int b = (u >> 31) ? (207 - c) : (272 + c);
;     if (sv == 0.0f) b = 208 + zi;
;     return b;
; template <int STAGE>
; __device__ __forceinline__ void pass2(LAS unsigned char* lds, const bf16* kbase, int g, int t0, const bf16x8 (&qf)[4][4], const f32x4 lo4, const f32x4 hi4, int wave, int r, int h2) {
;     ...
;         for (int hd = 0; hd < 4; ++hd) {
;             acc[hd] = f32x16{};
; #pragma unroll
;             for (int s = 0; s < 4; ++s) acc[hd] = __builtin_amdgcn_mfma_f32_32x32x16_bf16(WN ? kn[s] : kf[s], qf[hd][s], acc[hd], 0, 0, 0);
;         }
;         const int zi = (8191 - 32 * kt) >> 7;
;         const int lim = tq - 32 * kt - 4 * h2;
;         unsigned gtw = 0u, eqw = 0u;
;         float svq[16];
; #pragma unroll
;         for (int rg = 0; rg < 16; ++rg) {
;             const int c0 = att::crow(rg, 0);
;             float sv = fsum4_s(__builtin_amdgcn_fmed3f(acc[0][rg], lo4.x, hi4.x), __builtin_amdgcn_fmed3f(acc[1][rg], lo4.y, hi4.y),
;                                __builtin_amdgcn_fmed3f(acc[2][rg], lo4.z, hi4.z), __builtin_amdgcn_fmed3f(acc[3][rg], lo4.w, hi4.w));
;             const int b = bin2(sv, zi);
;             const bool valid = !DIAG || c0 <= lim;
;             if (STAGE == 0) {
;                 atomicAdd((unsigned*)&hist[r * HROW2 + (valid ? b : NB2)], 1u);
.LBB0_787:
	s_add_i32 s4, s0, s1
	s_cmp_lg_u32 s4, 16
	s_cbranch_scc0 .LBB0_793
	s_waitcnt vmcnt(3)
	v_mfma_f32_32x32x16_bf16 v[0:15], v[140:143], v[64:67], 0
	s_lshr_b32 s4, s6, 7
	s_addk_i32 s4, 0xd0
	v_mfma_f32_32x32x16_bf16 v[16:31], v[140:143], v[80:83], 0
	v_mfma_f32_32x32x16_bf16 v[32:47], v[140:143], v[96:99], 0
	v_mfma_f32_32x32x16_bf16 v[48:63], v[140:143], v[112:115], 0
	s_waitcnt vmcnt(2)
	v_mfma_f32_32x32x16_bf16 v[0:15], v[136:139], v[68:71], v[0:15]
	v_mfma_f32_32x32x16_bf16 v[16:31], v[136:139], v[84:87], v[16:31]
	v_mfma_f32_32x32x16_bf16 v[32:47], v[136:139], v[100:103], v[32:47]
	v_mfma_f32_32x32x16_bf16 v[48:63], v[136:139], v[116:119], v[48:63]
	s_waitcnt vmcnt(1)
	v_mfma_f32_32x32x16_bf16 v[0:15], v[132:135], v[72:75], v[0:15]
	v_mfma_f32_32x32x16_bf16 v[16:31], v[132:135], v[88:91], v[16:31]
	v_mfma_f32_32x32x16_bf16 v[32:47], v[132:135], v[104:107], v[32:47]
	v_mfma_f32_32x32x16_bf16 v[48:63], v[132:135], v[120:123], v[48:63]
	s_waitcnt vmcnt(0)
	v_mfma_f32_32x32x16_bf16 v[0:15], v[128:131], v[76:79], v[0:15]
	v_mfma_f32_32x32x16_bf16 v[16:31], v[128:131], v[92:95], v[16:31]
	s_nop 10
	v_med3_f32 v0, v0, v207, v208
	v_mfma_f32_32x32x16_bf16 v[32:47], v[128:131], v[108:111], v[32:47]
	v_med3_f32 v16, v16, v209, v210
	v_mfma_f32_32x32x16_bf16 v[48:63], v[128:131], v[124:127], v[48:63]
	s_nop 9
	v_med3_f32 v32, v32, v212, v213
	s_nop 0
	v_med3_f32 v48, v48, v214, v215
	v_add_f32 v160, v0, v16
	v_add_f32 v161, v32, v48
	v_add_f32 v160, v160, v161
	v_med3_f32 v32, v49, v214, v215
	v_bfe_u32 v0, v160, 20, 11
	v_med3_u32 v0, v0, s91, v190
	v_sub_u32_e32 v16, 0x40f, v0
	v_add_u32_e32 v0, 0xfffffdd0, v0
	v_cmp_gt_i32_e32 vcc, 0, v160
	s_nop 1
	v_cndmask_b32_e32 v0, v0, v16, vcc
	v_mov_b32_e32 v16, s4
	v_cmp_eq_f32_e32 vcc, 0, v160
	s_mov_b64 s[4:5], -1
	s_nop 0
	v_cndmask_b32_e32 v0, v0, v16, vcc
	v_lshl_add_u32 v0, v0, 2, v204
	ds_add_u32 v0, v184
	v_med3_f32 v0, v1, v207, v208
	v_med3_f32 v1, v17, v209, v210
	v_med3_f32 v17, v33, v212, v213
	v_add_f32 v33, v0, v1
	v_add_f32 v48, v17, v32
	v_add_f32 v33, v33, v48
	v_med3_f32 v17, v50, v214, v215
	v_bfe_u32 v0, v33, 20, 11
	v_med3_u32 v0, v0, s91, v190
	v_sub_u32_e32 v1, 0x40f, v0
	v_add_u32_e32 v0, 0xfffffdd0, v0
	v_cmp_gt_i32_e64 s[98:99], 0, v33
	v_cmp_eq_f32_e32 vcc, 0, v33
	s_nop 0
	v_cndmask_b32_e64 v0, v0, v1, s[98:99]
	v_med3_f32 v1, v18, v209, v210
	v_cndmask_b32_e32 v0, v0, v16, vcc
	v_lshl_add_u32 v0, v0, 2, v204
	ds_add_u32 v0, v184
	v_med3_f32 v0, v2, v207, v208
	v_med3_f32 v2, v34, v212, v213
	v_add_f32 v18, v0, v1
	v_add_f32 v32, v2, v17
	v_add_f32 v18, v18, v32
	v_med3_f32 v2, v35, v212, v213
	v_bfe_u32 v0, v18, 20, 11
	v_med3_u32 v0, v0, s91, v190
	v_sub_u32_e32 v1, 0x40f, v0
	v_add_u32_e32 v0, 0xfffffdd0, v0
	v_cmp_gt_i32_e64 s[98:99], 0, v18
	v_cmp_eq_f32_e32 vcc, 0, v18
	s_nop 0
	v_cndmask_b32_e64 v0, v0, v1, s[98:99]
	v_med3_f32 v1, v19, v209, v210
	v_cndmask_b32_e32 v0, v0, v16, vcc
	v_lshl_add_u32 v0, v0, 2, v204
	ds_add_u32 v0, v184
	v_med3_f32 v0, v3, v207, v208
	v_med3_f32 v3, v51, v214, v215
	v_add_f32 v17, v0, v1
	v_add_f32 v18, v2, v3
	v_add_f32 v17, v17, v18
	v_med3_f32 v2, v36, v212, v213
	v_bfe_u32 v0, v17, 20, 11
	v_med3_u32 v0, v0, s91, v190
	v_sub_u32_e32 v1, 0x40f, v0
	v_add_u32_e32 v0, 0xfffffdd0, v0
	v_cmp_gt_i32_e64 s[98:99], 0, v17
	v_cmp_eq_f32_e32 vcc, 0, v17
	v_med3_f32 v3, v52, v214, v215
	v_cndmask_b32_e64 v0, v0, v1, s[98:99]
	v_med3_f32 v1, v20, v209, v210
	v_cndmask_b32_e32 v0, v0, v16, vcc
	v_lshl_add_u32 v0, v0, 2, v204
	ds_add_u32 v0, v184
	v_med3_f32 v0, v4, v207, v208
	v_add_f32 v4, v0, v1
	v_add_f32 v17, v2, v3
	v_add_f32 v4, v4, v17
	v_med3_f32 v2, v37, v212, v213
	v_bfe_u32 v0, v4, 20, 11
	v_med3_u32 v0, v0, s91, v190
	v_sub_u32_e32 v1, 0x40f, v0
	v_add_u32_e32 v0, 0xfffffdd0, v0
	v_cmp_gt_i32_e64 s[98:99], 0, v4
	v_cmp_eq_f32_e32 vcc, 0, v4
	v_med3_f32 v3, v53, v214, v215
	v_cndmask_b32_e64 v0, v0, v1, s[98:99]
	v_med3_f32 v1, v21, v209, v210
	v_cndmask_b32_e32 v0, v0, v16, vcc
	v_lshl_add_u32 v0, v0, 2, v204
	ds_add_u32 v0, v184
	v_med3_f32 v0, v5, v207, v208
	v_add_f32 v4, v0, v1
	v_add_f32 v5, v2, v3
	v_add_f32 v4, v4, v5
	v_med3_f32 v2, v38, v212, v213
	v_bfe_u32 v0, v4, 20, 11
	v_med3_u32 v0, v0, s91, v190
	v_sub_u32_e32 v1, 0x40f, v0
	v_add_u32_e32 v0, 0xfffffdd0, v0
	v_cmp_gt_i32_e64 s[98:99], 0, v4
	v_cmp_eq_f32_e32 vcc, 0, v4
	v_med3_f32 v3, v54, v214, v215
	v_cndmask_b32_e64 v0, v0, v1, s[98:99]
	v_med3_f32 v1, v22, v209, v210
	v_cndmask_b32_e32 v0, v0, v16, vcc
	v_lshl_add_u32 v0, v0, 2, v204
	ds_add_u32 v0, v184
	v_med3_f32 v0, v6, v207, v208
	v_add_f32 v4, v0, v1
	v_add_f32 v5, v2, v3
	v_add_f32 v4, v4, v5
	v_med3_f32 v2, v39, v212, v213
	v_bfe_u32 v0, v4, 20, 11
	v_med3_u32 v0, v0, s91, v190
	v_sub_u32_e32 v1, 0x40f, v0
	v_add_u32_e32 v0, 0xfffffdd0, v0
	v_cmp_gt_i32_e64 s[98:99], 0, v4
	v_cmp_eq_f32_e32 vcc, 0, v4
	v_med3_f32 v3, v55, v214, v215
	v_cndmask_b32_e64 v0, v0, v1, s[98:99]
	v_med3_f32 v1, v23, v209, v210
	v_cndmask_b32_e32 v0, v0, v16, vcc
	v_lshl_add_u32 v0, v0, 2, v204
	ds_add_u32 v0, v184
	v_med3_f32 v0, v7, v207, v208
	v_add_f32 v4, v0, v1
	v_add_f32 v5, v2, v3
	v_add_f32 v4, v4, v5
	v_med3_f32 v2, v40, v212, v213
	v_bfe_u32 v0, v4, 20, 11
	v_med3_u32 v0, v0, s91, v190
	v_sub_u32_e32 v1, 0x40f, v0
	v_add_u32_e32 v0, 0xfffffdd0, v0
	v_cmp_gt_i32_e64 s[98:99], 0, v4
	v_cmp_eq_f32_e32 vcc, 0, v4
	v_med3_f32 v3, v56, v214, v215
	v_cndmask_b32_e64 v0, v0, v1, s[98:99]
	v_med3_f32 v1, v24, v209, v210
	v_cndmask_b32_e32 v0, v0, v16, vcc
	v_lshl_add_u32 v0, v0, 2, v204
	ds_add_u32 v0, v184
	v_med3_f32 v0, v8, v207, v208
	v_add_f32 v4, v0, v1
	v_add_f32 v5, v2, v3
	v_add_f32 v4, v4, v5
; __device__ __forceinline__ int crow(int reg, int h) { return (reg & 3) + 8 * (reg >> 2) + 4 * h; }
; #define DSA2_LOADK(dst, kt_) do { _Pragma("unroll") for (int s = 0; s < 4; ++s) dst[s] = *(const bf16x8*)(kp + (size_t)(32 * (kt_)) * Y0P + 16 * s); } while (0)
; template <int STAGE>
; __device__ __forceinline__ void pass2(LAS unsigned char* lds, const bf16* kbase, int g, int t0, const bf16x8 (&qf)[4][4], const f32x4 lo4, const f32x4 hi4, int wave, int r, int h2) {
;     ...
;         for (int rg = 0; rg < 16; ++rg) {
;             const int c0 = att::crow(rg, 0);
;             float sv = fsum4_s(__builtin_amdgcn_fmed3f(acc[0][rg], lo4.x, hi4.x), __builtin_amdgcn_fmed3f(acc[1][rg], lo4.y, hi4.y),
;                                __builtin_amdgcn_fmed3f(acc[2][rg], lo4.z, hi4.z), __builtin_amdgcn_fmed3f(acc[3][rg], lo4.w, hi4.w));
;             const int b = bin2(sv, zi);
;             const bool valid = !DIAG || c0 <= lim;
;             if (STAGE == 0) {
;                 atomicAdd((unsigned*)&hist[r * HROW2 + (valid ? b : NB2)], 1u);
;     ...
;     for (;;) {
;         if (kt > g) break;
;         if (kt + 8 <= g) DSA2_LOADK(kn, kt + 8);
;         if (kt == g) { tile(pg8::BoolC2<false>{}, kt, pg8::BoolC2<true>{}); break; }
;         tile(pg8::BoolC2<false>{}, kt, pg8::BoolC2<false>{});
;         kt += 8;
;         if (kt > g) break;
;         if (kt + 8 <= g) DSA2_LOADK(kf, kt + 8);
	v_med3_f32 v2, v41, v212, v213
	v_bfe_u32 v0, v4, 20, 11
	v_med3_u32 v0, v0, s91, v190
	v_sub_u32_e32 v1, 0x40f, v0
	v_add_u32_e32 v0, 0xfffffdd0, v0
	v_cmp_gt_i32_e64 s[98:99], 0, v4
	v_cmp_eq_f32_e32 vcc, 0, v4
	v_med3_f32 v3, v57, v214, v215
	v_cndmask_b32_e64 v0, v0, v1, s[98:99]
	v_med3_f32 v1, v25, v209, v210
	v_cndmask_b32_e32 v0, v0, v16, vcc
	v_lshl_add_u32 v0, v0, 2, v204
	ds_add_u32 v0, v184
	v_med3_f32 v0, v9, v207, v208
	v_add_f32 v4, v0, v1
	v_add_f32 v5, v2, v3
	v_add_f32 v4, v4, v5
	v_med3_f32 v2, v42, v212, v213
	v_bfe_u32 v0, v4, 20, 11
	v_med3_u32 v0, v0, s91, v190
	v_sub_u32_e32 v1, 0x40f, v0
	v_add_u32_e32 v0, 0xfffffdd0, v0
	v_cmp_gt_i32_e64 s[98:99], 0, v4
	v_cmp_eq_f32_e32 vcc, 0, v4
	v_med3_f32 v3, v58, v214, v215
	v_cndmask_b32_e64 v0, v0, v1, s[98:99]
	v_med3_f32 v1, v26, v209, v210
	v_cndmask_b32_e32 v0, v0, v16, vcc
	v_lshl_add_u32 v0, v0, 2, v204
	ds_add_u32 v0, v184
	v_med3_f32 v0, v10, v207, v208
	v_add_f32 v4, v0, v1
	v_add_f32 v5, v2, v3
	v_add_f32 v4, v4, v5
	v_med3_f32 v2, v43, v212, v213
	v_bfe_u32 v0, v4, 20, 11
	v_med3_u32 v0, v0, s91, v190
	v_sub_u32_e32 v1, 0x40f, v0
	v_add_u32_e32 v0, 0xfffffdd0, v0
	v_cmp_gt_i32_e64 s[98:99], 0, v4
	v_cmp_eq_f32_e32 vcc, 0, v4
	v_med3_f32 v3, v59, v214, v215
	v_cndmask_b32_e64 v0, v0, v1, s[98:99]
	v_med3_f32 v1, v27, v209, v210
	v_cndmask_b32_e32 v0, v0, v16, vcc
	v_lshl_add_u32 v0, v0, 2, v204
	ds_add_u32 v0, v184
	v_med3_f32 v0, v11, v207, v208
	v_add_f32 v4, v0, v1
	v_add_f32 v5, v2, v3
	v_add_f32 v4, v4, v5
	v_med3_f32 v2, v44, v212, v213
	v_bfe_u32 v0, v4, 20, 11
	v_med3_u32 v0, v0, s91, v190
	v_sub_u32_e32 v1, 0x40f, v0
	v_add_u32_e32 v0, 0xfffffdd0, v0
	v_cmp_gt_i32_e64 s[98:99], 0, v4
	v_cmp_eq_f32_e32 vcc, 0, v4
	v_med3_f32 v3, v60, v214, v215
	v_cndmask_b32_e64 v0, v0, v1, s[98:99]
	v_med3_f32 v1, v28, v209, v210
	v_cndmask_b32_e32 v0, v0, v16, vcc
	v_lshl_add_u32 v0, v0, 2, v204
	ds_add_u32 v0, v184
	v_med3_f32 v0, v12, v207, v208
	v_add_f32 v4, v0, v1
	v_add_f32 v5, v2, v3
	v_add_f32 v4, v4, v5
	v_med3_f32 v2, v45, v212, v213
	v_bfe_u32 v0, v4, 20, 11
	v_med3_u32 v0, v0, s91, v190
	v_sub_u32_e32 v1, 0x40f, v0
	v_add_u32_e32 v0, 0xfffffdd0, v0
	v_cmp_gt_i32_e64 s[98:99], 0, v4
	v_cmp_eq_f32_e32 vcc, 0, v4
	v_med3_f32 v3, v61, v214, v215
	v_cndmask_b32_e64 v0, v0, v1, s[98:99]
	v_med3_f32 v1, v29, v209, v210
	v_cndmask_b32_e32 v0, v0, v16, vcc
	v_lshl_add_u32 v0, v0, 2, v204
	ds_add_u32 v0, v184
	v_med3_f32 v0, v13, v207, v208
	v_add_f32 v4, v0, v1
	v_add_f32 v5, v2, v3
	v_add_f32 v4, v4, v5
	v_med3_f32 v2, v46, v212, v213
	v_bfe_u32 v0, v4, 20, 11
	v_med3_u32 v0, v0, s91, v190
	v_sub_u32_e32 v1, 0x40f, v0
	v_add_u32_e32 v0, 0xfffffdd0, v0
	v_cmp_gt_i32_e64 s[98:99], 0, v4
	v_cmp_eq_f32_e32 vcc, 0, v4
	v_med3_f32 v3, v62, v214, v215
	v_cndmask_b32_e64 v0, v0, v1, s[98:99]
	v_med3_f32 v1, v30, v209, v210
	v_cndmask_b32_e32 v0, v0, v16, vcc
	v_lshl_add_u32 v0, v0, 2, v204
	ds_add_u32 v0, v184
	v_med3_f32 v0, v14, v207, v208
	v_add_f32 v4, v0, v1
	v_add_f32 v5, v2, v3
	v_add_f32 v4, v4, v5
	v_med3_f32 v2, v47, v212, v213
	v_bfe_u32 v0, v4, 20, 11
	v_med3_u32 v0, v0, s91, v190
	v_sub_u32_e32 v1, 0x40f, v0
	v_add_u32_e32 v0, 0xfffffdd0, v0
	v_cmp_gt_i32_e64 s[98:99], 0, v4
	v_cmp_eq_f32_e32 vcc, 0, v4
	v_med3_f32 v3, v63, v214, v215
	v_cndmask_b32_e64 v0, v0, v1, s[98:99]
	v_med3_f32 v1, v31, v209, v210
	v_cndmask_b32_e32 v0, v0, v16, vcc
	v_lshl_add_u32 v0, v0, 2, v204
	ds_add_u32 v0, v184
	v_med3_f32 v0, v15, v207, v208
	v_add_f32 v4, v0, v1
	v_add_f32 v5, v2, v3
	v_add_f32 v4, v4, v5
	s_nop 0
	v_bfe_u32 v0, v4, 20, 11
	v_med3_u32 v0, v0, s91, v190
	v_sub_u32_e32 v1, 0x40f, v0
	v_add_u32_e32 v0, 0xfffffdd0, v0
	v_cmp_gt_i32_e64 s[98:99], 0, v4
	v_cmp_eq_f32_e32 vcc, 0, v4
	s_nop 0
	v_cndmask_b32_e64 v0, v0, v1, s[98:99]
	v_cndmask_b32_e32 v0, v0, v16, vcc
	v_lshl_add_u32 v0, v0, 2, v204
	ds_add_u32 v0, v184
	s_and_b64 vcc, exec, s[2:3]
	s_mov_b64 s[2:3], -1
	s_cbranch_vccz .LBB0_794
	s_cmp_gt_u32 s1, s64
	s_cselect_b64 s[2:3], -1, 0
	v_mov_b64_e32 v[174:175], v[130:131]
	v_mov_b64_e32 v[170:171], v[134:135]
	v_mov_b64_e32 v[166:167], v[138:139]
	v_mov_b64_e32 v[162:163], v[142:143]
	s_and_b64 vcc, exec, s[2:3]
	v_mov_b64_e32 v[172:173], v[128:129]
	v_mov_b64_e32 v[168:169], v[132:133]
	v_mov_b64_e32 v[164:165], v[136:137]
	v_mov_b64_e32 v[160:161], v[140:141]
	s_cbranch_vccnz .LBB0_791
	global_load_dwordx4 v[160:163], v[180:181], off offset:-96
	global_load_dwordx4 v[164:167], v[180:181], off offset:-64
	global_load_dwordx4 v[168:171], v[180:181], off offset:-32
	global_load_dwordx4 v[172:175], v[180:181], off
; __device__ __forceinline__ int crow(int reg, int h) { return (reg & 3) + 8 * (reg >> 2) + 4 * h; }
; __device__ __forceinline__ int bin2(float sv, int zi) {
;     const unsigned u = __float_as_uint(sv);
;     int c = (int)((u >> 20) & 0x7FFu) - 832;
;     c = c < 0 ? 0 : (c > 207 ? 207 : c);
;     int b = (u >> 31) ? (207 - c) : (272 + c);
;     if (sv == 0.0f) b = 208 + zi;
;     return b;
; template <int STAGE>
; __device__ __forceinline__ void pass2(LAS unsigned char* lds, const bf16* kbase, int g, int t0, const bf16x8 (&qf)[4][4], const f32x4 lo4, const f32x4 hi4, int wave, int r, int h2) {
;     ...
;         for (int hd = 0; hd < 4; ++hd) {
;             acc[hd] = f32x16{};
; #pragma unroll
;             for (int s = 0; s < 4; ++s) acc[hd] = __builtin_amdgcn_mfma_f32_32x32x16_bf16(WN ? kn[s] : kf[s], qf[hd][s], acc[hd], 0, 0, 0);
;         }
;         const int zi = (8191 - 32 * kt) >> 7;
;         const int lim = tq - 32 * kt - 4 * h2;
;         unsigned gtw = 0u, eqw = 0u;
;         float svq[16];
; #pragma unroll
;         for (int rg = 0; rg < 16; ++rg) {
;             const int c0 = att::crow(rg, 0);
;             float sv = fsum4_s(__builtin_amdgcn_fmed3f(acc[0][rg], lo4.x, hi4.x), __builtin_amdgcn_fmed3f(acc[1][rg], lo4.y, hi4.y),
;                                __builtin_amdgcn_fmed3f(acc[2][rg], lo4.z, hi4.z), __builtin_amdgcn_fmed3f(acc[3][rg], lo4.w, hi4.w));
;             const int b = bin2(sv, zi);
;             const bool valid = !DIAG || c0 <= lim;
;             if (STAGE == 0) {
;                 atomicAdd((unsigned*)&hist[r * HROW2 + (valid ? b : NB2)], 1u);
.LBB0_791:
	s_add_i32 s1, s1, 16
	s_add_i32 s4, s0, s1
	s_cmp_lg_u32 s4, 24
	s_cbranch_scc0 .LBB0_795
	v_mfma_f32_32x32x16_bf16 v[0:15], v[156:159], v[64:67], 0
	s_add_i32 s4, s6, 0xffffff00
	s_lshr_b32 s4, s4, 7
	s_addk_i32 s4, 0xd0
	s_addk_i32 s6, 0xfe00
	s_mov_b64 s[8:9], 0
	v_mfma_f32_32x32x16_bf16 v[16:31], v[156:159], v[80:83], 0
	v_mfma_f32_32x32x16_bf16 v[32:47], v[156:159], v[96:99], 0
	v_mfma_f32_32x32x16_bf16 v[48:63], v[156:159], v[112:115], 0
	v_mfma_f32_32x32x16_bf16 v[0:15], v[152:155], v[68:71], v[0:15]
	v_mfma_f32_32x32x16_bf16 v[16:31], v[152:155], v[84:87], v[16:31]
	v_mfma_f32_32x32x16_bf16 v[32:47], v[152:155], v[100:103], v[32:47]
	v_mfma_f32_32x32x16_bf16 v[48:63], v[152:155], v[116:119], v[48:63]
	v_mfma_f32_32x32x16_bf16 v[0:15], v[148:151], v[72:75], v[0:15]
	v_mfma_f32_32x32x16_bf16 v[16:31], v[148:151], v[88:91], v[16:31]
	v_mfma_f32_32x32x16_bf16 v[32:47], v[148:151], v[104:107], v[32:47]
	v_mfma_f32_32x32x16_bf16 v[48:63], v[148:151], v[120:123], v[48:63]
	v_mfma_f32_32x32x16_bf16 v[0:15], v[144:147], v[76:79], v[0:15]
	v_mfma_f32_32x32x16_bf16 v[16:31], v[144:147], v[92:95], v[16:31]
	s_nop 10
	v_med3_f32 v0, v0, v207, v208
	v_mfma_f32_32x32x16_bf16 v[32:47], v[144:147], v[108:111], v[32:47]
	v_med3_f32 v16, v16, v209, v210
	v_mfma_f32_32x32x16_bf16 v[48:63], v[144:147], v[124:127], v[48:63]
	s_nop 9
	v_med3_f32 v32, v32, v212, v213
	s_nop 0
	v_med3_f32 v48, v48, v214, v215
	v_add_f32 v176, v0, v16
	v_add_f32 v205, v32, v48
	v_add_f32 v176, v176, v205
	v_med3_f32 v32, v49, v214, v215
	v_bfe_u32 v0, v176, 20, 11
	v_med3_u32 v0, v0, s91, v190
	v_sub_u32_e32 v16, 0x40f, v0
	v_add_u32_e32 v0, 0xfffffdd0, v0
	v_cmp_gt_i32_e32 vcc, 0, v176
	s_nop 1
	v_cndmask_b32_e32 v0, v0, v16, vcc
	v_mov_b32_e32 v16, s4
	v_cmp_eq_f32_e32 vcc, 0, v176
	s_mov_b64 s[4:5], 0x380000
	v_lshl_add_u64 v[180:181], v[180:181], 0, s[4:5]
	v_cndmask_b32_e32 v0, v0, v16, vcc
	v_lshl_add_u32 v0, v0, 2, v204
	ds_add_u32 v0, v184
	v_med3_f32 v0, v1, v207, v208
	v_med3_f32 v1, v17, v209, v210
	v_med3_f32 v17, v33, v212, v213
	v_add_f32 v33, v0, v1
	v_add_f32 v48, v17, v32
	v_add_f32 v33, v33, v48
	v_med3_f32 v17, v50, v214, v215
	v_bfe_u32 v0, v33, 20, 11
	v_med3_u32 v0, v0, s91, v190
	v_sub_u32_e32 v1, 0x40f, v0
	v_add_u32_e32 v0, 0xfffffdd0, v0
	v_cmp_gt_i32_e64 s[98:99], 0, v33
	v_cmp_eq_f32_e32 vcc, 0, v33
	s_mov_b64 s[4:5], -1
	v_cndmask_b32_e64 v0, v0, v1, s[98:99]
	v_med3_f32 v1, v18, v209, v210
	v_cndmask_b32_e32 v0, v0, v16, vcc
	v_lshl_add_u32 v0, v0, 2, v204
	ds_add_u32 v0, v184
	v_med3_f32 v0, v2, v207, v208
	v_med3_f32 v2, v34, v212, v213
	v_add_f32 v18, v0, v1
	v_add_f32 v32, v2, v17
	v_add_f32 v18, v18, v32
	v_med3_f32 v2, v35, v212, v213
	v_bfe_u32 v0, v18, 20, 11
	v_med3_u32 v0, v0, s91, v190
	v_sub_u32_e32 v1, 0x40f, v0
	v_add_u32_e32 v0, 0xfffffdd0, v0
	v_cmp_gt_i32_e64 s[98:99], 0, v18
	v_cmp_eq_f32_e32 vcc, 0, v18
	s_nop 0
	v_cndmask_b32_e64 v0, v0, v1, s[98:99]
	v_med3_f32 v1, v19, v209, v210
	v_cndmask_b32_e32 v0, v0, v16, vcc
	v_lshl_add_u32 v0, v0, 2, v204
	ds_add_u32 v0, v184
	v_med3_f32 v0, v3, v207, v208
	v_med3_f32 v3, v51, v214, v215
	v_add_f32 v17, v0, v1
	v_add_f32 v18, v2, v3
	v_add_f32 v17, v17, v18
	v_med3_f32 v2, v36, v212, v213
	v_bfe_u32 v0, v17, 20, 11
	v_med3_u32 v0, v0, s91, v190
	v_sub_u32_e32 v1, 0x40f, v0
	v_add_u32_e32 v0, 0xfffffdd0, v0
	v_cmp_gt_i32_e64 s[98:99], 0, v17
	v_cmp_eq_f32_e32 vcc, 0, v17
	v_med3_f32 v3, v52, v214, v215
	v_cndmask_b32_e64 v0, v0, v1, s[98:99]
	v_med3_f32 v1, v20, v209, v210
	v_cndmask_b32_e32 v0, v0, v16, vcc
	v_lshl_add_u32 v0, v0, 2, v204
	ds_add_u32 v0, v184
	v_med3_f32 v0, v4, v207, v208
	v_add_f32 v4, v0, v1
	v_add_f32 v17, v2, v3
	v_add_f32 v4, v4, v17
	v_med3_f32 v2, v37, v212, v213
	v_bfe_u32 v0, v4, 20, 11
	v_med3_u32 v0, v0, s91, v190
	v_sub_u32_e32 v1, 0x40f, v0
	v_add_u32_e32 v0, 0xfffffdd0, v0
	v_cmp_gt_i32_e64 s[98:99], 0, v4
	v_cmp_eq_f32_e32 vcc, 0, v4
	v_med3_f32 v3, v53, v214, v215
	v_cndmask_b32_e64 v0, v0, v1, s[98:99]
	v_med3_f32 v1, v21, v209, v210
	v_cndmask_b32_e32 v0, v0, v16, vcc
	v_lshl_add_u32 v0, v0, 2, v204
	ds_add_u32 v0, v184
	v_med3_f32 v0, v5, v207, v208
	v_add_f32 v4, v0, v1
	v_add_f32 v5, v2, v3
	v_add_f32 v4, v4, v5
	v_med3_f32 v2, v38, v212, v213
	v_bfe_u32 v0, v4, 20, 11
	v_med3_u32 v0, v0, s91, v190
	v_sub_u32_e32 v1, 0x40f, v0
	v_add_u32_e32 v0, 0xfffffdd0, v0
	v_cmp_gt_i32_e64 s[98:99], 0, v4
	v_cmp_eq_f32_e32 vcc, 0, v4
	v_med3_f32 v3, v54, v214, v215
	v_cndmask_b32_e64 v0, v0, v1, s[98:99]
	v_med3_f32 v1, v22, v209, v210
	v_cndmask_b32_e32 v0, v0, v16, vcc
	v_lshl_add_u32 v0, v0, 2, v204
	ds_add_u32 v0, v184
	v_med3_f32 v0, v6, v207, v208
	v_add_f32 v4, v0, v1
	v_add_f32 v5, v2, v3
	v_add_f32 v4, v4, v5
	v_med3_f32 v2, v39, v212, v213
	v_bfe_u32 v0, v4, 20, 11
	v_med3_u32 v0, v0, s91, v190
	v_sub_u32_e32 v1, 0x40f, v0
; __device__ __forceinline__ int crow(int reg, int h) { return (reg & 3) + 8 * (reg >> 2) + 4 * h; }
; __device__ __forceinline__ int bin2(float sv, int zi) {
;     const unsigned u = __float_as_uint(sv);
;     int c = (int)((u >> 20) & 0x7FFu) - 832;
;     c = c < 0 ? 0 : (c > 207 ? 207 : c);
;     int b = (u >> 31) ? (207 - c) : (272 + c);
;     if (sv == 0.0f) b = 208 + zi;
;     return b;
; template <int STAGE>
; __device__ __forceinline__ void pass2(LAS unsigned char* lds, const bf16* kbase, int g, int t0, const bf16x8 (&qf)[4][4], const f32x4 lo4, const f32x4 hi4, int wave, int r, int h2) {
;     ...
;         for (int rg = 0; rg < 16; ++rg) {
;             const int c0 = att::crow(rg, 0);
;             float sv = fsum4_s(__builtin_amdgcn_fmed3f(acc[0][rg], lo4.x, hi4.x), __builtin_amdgcn_fmed3f(acc[1][rg], lo4.y, hi4.y),
;                                __builtin_amdgcn_fmed3f(acc[2][rg], lo4.z, hi4.z), __builtin_amdgcn_fmed3f(acc[3][rg], lo4.w, hi4.w));
;             const int b = bin2(sv, zi);
;             const bool valid = !DIAG || c0 <= lim;
;             if (STAGE == 0) {
;                 atomicAdd((unsigned*)&hist[r * HROW2 + (valid ? b : NB2)], 1u);
	v_add_u32_e32 v0, 0xfffffdd0, v0
	v_cmp_gt_i32_e64 s[98:99], 0, v4
	v_cmp_eq_f32_e32 vcc, 0, v4
	v_med3_f32 v3, v55, v214, v215
	v_cndmask_b32_e64 v0, v0, v1, s[98:99]
	v_med3_f32 v1, v23, v209, v210
	v_cndmask_b32_e32 v0, v0, v16, vcc
	v_lshl_add_u32 v0, v0, 2, v204
	ds_add_u32 v0, v184
	v_med3_f32 v0, v7, v207, v208
	v_add_f32 v4, v0, v1
	v_add_f32 v5, v2, v3
	v_add_f32 v4, v4, v5
	v_med3_f32 v2, v40, v212, v213
	v_bfe_u32 v0, v4, 20, 11
	v_med3_u32 v0, v0, s91, v190
	v_sub_u32_e32 v1, 0x40f, v0
	v_add_u32_e32 v0, 0xfffffdd0, v0
	v_cmp_gt_i32_e64 s[98:99], 0, v4
	v_cmp_eq_f32_e32 vcc, 0, v4
	v_med3_f32 v3, v56, v214, v215
	v_cndmask_b32_e64 v0, v0, v1, s[98:99]
	v_med3_f32 v1, v24, v209, v210
	v_cndmask_b32_e32 v0, v0, v16, vcc
	v_lshl_add_u32 v0, v0, 2, v204
	ds_add_u32 v0, v184
	v_med3_f32 v0, v8, v207, v208
	v_add_f32 v4, v0, v1
	v_add_f32 v5, v2, v3
	v_add_f32 v4, v4, v5
	v_med3_f32 v2, v41, v212, v213
	v_bfe_u32 v0, v4, 20, 11
	v_med3_u32 v0, v0, s91, v190
	v_sub_u32_e32 v1, 0x40f, v0
	v_add_u32_e32 v0, 0xfffffdd0, v0
	v_cmp_gt_i32_e64 s[98:99], 0, v4
	v_cmp_eq_f32_e32 vcc, 0, v4
	v_med3_f32 v3, v57, v214, v215
	v_cndmask_b32_e64 v0, v0, v1, s[98:99]
	v_med3_f32 v1, v25, v209, v210
	v_cndmask_b32_e32 v0, v0, v16, vcc
	v_lshl_add_u32 v0, v0, 2, v204
	ds_add_u32 v0, v184
	v_med3_f32 v0, v9, v207, v208
	v_add_f32 v4, v0, v1
	v_add_f32 v5, v2, v3
	v_add_f32 v4, v4, v5
	v_med3_f32 v2, v42, v212, v213
	v_bfe_u32 v0, v4, 20, 11
	v_med3_u32 v0, v0, s91, v190
	v_sub_u32_e32 v1, 0x40f, v0
	v_add_u32_e32 v0, 0xfffffdd0, v0
	v_cmp_gt_i32_e64 s[98:99], 0, v4
	v_cmp_eq_f32_e32 vcc, 0, v4
	v_med3_f32 v3, v58, v214, v215
	v_cndmask_b32_e64 v0, v0, v1, s[98:99]
	v_med3_f32 v1, v26, v209, v210
	v_cndmask_b32_e32 v0, v0, v16, vcc
	v_lshl_add_u32 v0, v0, 2, v204
	ds_add_u32 v0, v184
	v_med3_f32 v0, v10, v207, v208
	v_add_f32 v4, v0, v1
	v_add_f32 v5, v2, v3
	v_add_f32 v4, v4, v5
	v_med3_f32 v2, v43, v212, v213
	v_bfe_u32 v0, v4, 20, 11
	v_med3_u32 v0, v0, s91, v190
	v_sub_u32_e32 v1, 0x40f, v0
	v_add_u32_e32 v0, 0xfffffdd0, v0
	v_cmp_gt_i32_e64 s[98:99], 0, v4
	v_cmp_eq_f32_e32 vcc, 0, v4
	v_med3_f32 v3, v59, v214, v215
	v_cndmask_b32_e64 v0, v0, v1, s[98:99]
	v_med3_f32 v1, v27, v209, v210
	v_cndmask_b32_e32 v0, v0, v16, vcc
	v_lshl_add_u32 v0, v0, 2, v204
	ds_add_u32 v0, v184
	v_med3_f32 v0, v11, v207, v208
	v_add_f32 v4, v0, v1
	v_add_f32 v5, v2, v3
	v_add_f32 v4, v4, v5
	v_med3_f32 v2, v44, v212, v213
	v_bfe_u32 v0, v4, 20, 11
	v_med3_u32 v0, v0, s91, v190
	v_sub_u32_e32 v1, 0x40f, v0
	v_add_u32_e32 v0, 0xfffffdd0, v0
	v_cmp_gt_i32_e64 s[98:99], 0, v4
	v_cmp_eq_f32_e32 vcc, 0, v4
	v_med3_f32 v3, v60, v214, v215
	v_cndmask_b32_e64 v0, v0, v1, s[98:99]
	v_med3_f32 v1, v28, v209, v210
	v_cndmask_b32_e32 v0, v0, v16, vcc
	v_lshl_add_u32 v0, v0, 2, v204
	ds_add_u32 v0, v184
	v_med3_f32 v0, v12, v207, v208
	v_add_f32 v4, v0, v1
	v_add_f32 v5, v2, v3
	v_add_f32 v4, v4, v5
	v_med3_f32 v2, v45, v212, v213
	v_bfe_u32 v0, v4, 20, 11
	v_med3_u32 v0, v0, s91, v190
	v_sub_u32_e32 v1, 0x40f, v0
	v_add_u32_e32 v0, 0xfffffdd0, v0
	v_cmp_gt_i32_e64 s[98:99], 0, v4
	v_cmp_eq_f32_e32 vcc, 0, v4
	v_med3_f32 v3, v61, v214, v215
	v_cndmask_b32_e64 v0, v0, v1, s[98:99]
	v_med3_f32 v1, v29, v209, v210
	v_cndmask_b32_e32 v0, v0, v16, vcc
	v_lshl_add_u32 v0, v0, 2, v204
	ds_add_u32 v0, v184
	v_med3_f32 v0, v13, v207, v208
	v_add_f32 v4, v0, v1
	v_add_f32 v5, v2, v3
	v_add_f32 v4, v4, v5
	v_med3_f32 v2, v46, v212, v213
	v_bfe_u32 v0, v4, 20, 11
	v_med3_u32 v0, v0, s91, v190
	v_sub_u32_e32 v1, 0x40f, v0
	v_add_u32_e32 v0, 0xfffffdd0, v0
	v_cmp_gt_i32_e64 s[98:99], 0, v4
	v_cmp_eq_f32_e32 vcc, 0, v4
	v_med3_f32 v3, v62, v214, v215
	v_cndmask_b32_e64 v0, v0, v1, s[98:99]
	v_med3_f32 v1, v30, v209, v210
	v_cndmask_b32_e32 v0, v0, v16, vcc
	v_lshl_add_u32 v0, v0, 2, v204
	ds_add_u32 v0, v184
	v_med3_f32 v0, v14, v207, v208
	v_add_f32 v4, v0, v1
	v_add_f32 v5, v2, v3
	v_add_f32 v4, v4, v5
	v_med3_f32 v2, v47, v212, v213
	v_bfe_u32 v0, v4, 20, 11
	v_med3_u32 v0, v0, s91, v190
	v_sub_u32_e32 v1, 0x40f, v0
	v_add_u32_e32 v0, 0xfffffdd0, v0
	v_cmp_gt_i32_e64 s[98:99], 0, v4
	v_cmp_eq_f32_e32 vcc, 0, v4
	v_med3_f32 v3, v63, v214, v215
	v_cndmask_b32_e64 v0, v0, v1, s[98:99]
	v_med3_f32 v1, v31, v209, v210
	v_cndmask_b32_e32 v0, v0, v16, vcc
	v_lshl_add_u32 v0, v0, 2, v204
	ds_add_u32 v0, v184
	v_med3_f32 v0, v15, v207, v208
	v_add_f32 v4, v0, v1
	v_add_f32 v5, v2, v3
	v_add_f32 v4, v4, v5
	s_nop 0
	v_bfe_u32 v0, v4, 20, 11
	v_med3_u32 v0, v0, s91, v190
	v_sub_u32_e32 v1, 0x40f, v0
	v_add_u32_e32 v0, 0xfffffdd0, v0
	v_cmp_gt_i32_e64 s[98:99], 0, v4
	v_cmp_eq_f32_e32 vcc, 0, v4
	s_nop 0
	v_cndmask_b32_e64 v0, v0, v1, s[98:99]
	v_cndmask_b32_e32 v0, v0, v16, vcc
	v_lshl_add_u32 v0, v0, 2, v204
	ds_add_u32 v0, v184
	s_and_b64 vcc, exec, s[2:3]
	s_cbranch_vccz .LBB0_796
	s_branch .LBB0_797

; #define LAS __attribute__((address_space(3)))
; __device__ __forceinline__ int crow(int reg, int h) { return (reg & 3) + 8 * (reg >> 2) + 4 * h; }
; template <int STAGE>
; __device__ __forceinline__ void pass2(LAS unsigned char* lds, const bf16* kbase, int g, int t0, const bf16x8 (&qf)[4][4], const f32x4 lo4, const f32x4 hi4, int wave, int r, int h2) {
;     ...
;         for (int hd = 0; hd < 4; ++hd) {
;             acc[hd] = f32x16{};
; #pragma unroll
;             for (int s = 0; s < 4; ++s) acc[hd] = __builtin_amdgcn_mfma_f32_32x32x16_bf16(WN ? kn[s] : kf[s], qf[hd][s], acc[hd], 0, 0, 0);
;         }
;         const int zi = (8191 - 32 * kt) >> 7;
;         const int lim = tq - 32 * kt - 4 * h2;
;         unsigned gtw = 0u, eqw = 0u;
;         float svq[16];
; #pragma unroll
;         for (int rg = 0; rg < 16; ++rg) {
;             const int c0 = att::crow(rg, 0);
;             float sv = fsum4_s(__builtin_amdgcn_fmed3f(acc[0][rg], lo4.x, hi4.x), __builtin_amdgcn_fmed3f(acc[1][rg], lo4.y, hi4.y),
;                                __builtin_amdgcn_fmed3f(acc[2][rg], lo4.z, hi4.z), __builtin_amdgcn_fmed3f(acc[3][rg], lo4.w, hi4.w));
;             const int b = bin2(sv, zi);
;             const bool valid = !DIAG || c0 <= lim;
;             if (STAGE == 0) {
;                 atomicAdd((unsigned*)&hist[r * HROW2 + (valid ? b : NB2)], 1u);
;             } else {
;                 if (valid && b > tb) gtw |= 1u << c0;
;                 if (valid && b == tb) eqw |= 1u << c0;
;                 svq[rg] = sv;
;             }
;         }
;         if (STAGE == 1) {
;             LAS unsigned char* st = lds + OFF2_SV + wave * 4096 + (r + 32 * h2) * 16;
; #pragma unroll
;             for (int q = 0; q < 4; ++q) *(LAS f32x4*)(st + q * 1024) = (f32x4){svq[4 * q], svq[4 * q + 1], svq[4 * q + 2], svq[4 * q + 3]};
.LBB0_826:
	s_cmp_lg_u32 s0, s64
	s_cbranch_scc0 .LBB0_852
	s_waitcnt vmcnt(3)
	v_mfma_f32_32x32x16_bf16 v[0:15], v[140:143], v[64:67], 0
	s_lshl_b32 s6, s0, 5
	s_sub_i32 s7, 0x1fe0, s6
	s_lshr_b32 s7, s7, 7
	s_addk_i32 s7, 0xd0
	v_mfma_f32_32x32x16_bf16 v[16:31], v[140:143], v[80:83], 0
	v_mfma_f32_32x32x16_bf16 v[32:47], v[140:143], v[96:99], 0
	v_mfma_f32_32x32x16_bf16 v[48:63], v[140:143], v[112:115], 0
	s_waitcnt vmcnt(2)
	v_mfma_f32_32x32x16_bf16 v[0:15], v[136:139], v[68:71], v[0:15]
	v_mfma_f32_32x32x16_bf16 v[16:31], v[136:139], v[84:87], v[16:31]
	v_mfma_f32_32x32x16_bf16 v[32:47], v[136:139], v[100:103], v[32:47]
	v_mfma_f32_32x32x16_bf16 v[48:63], v[136:139], v[116:119], v[48:63]
	s_waitcnt vmcnt(1)
	v_mfma_f32_32x32x16_bf16 v[0:15], v[132:135], v[72:75], v[0:15]
	v_mfma_f32_32x32x16_bf16 v[16:31], v[132:135], v[88:91], v[16:31]
	v_mfma_f32_32x32x16_bf16 v[32:47], v[132:135], v[104:107], v[32:47]
	v_mfma_f32_32x32x16_bf16 v[48:63], v[132:135], v[120:123], v[48:63]
	s_waitcnt vmcnt(0)
	v_mfma_f32_32x32x16_bf16 v[0:15], v[128:131], v[76:79], v[0:15]
	v_mfma_f32_32x32x16_bf16 v[16:31], v[128:131], v[92:95], v[16:31]
	s_nop 10
	v_med3_f32 v0, v0, v207, v208
	v_med3_f32 v1, v1, v207, v208
	v_mfma_f32_32x32x16_bf16 v[32:47], v[128:131], v[108:111], v[32:47]
	v_med3_f32 v16, v16, v209, v210
	v_mfma_f32_32x32x16_bf16 v[48:63], v[128:131], v[124:127], v[48:63]
	s_nop 9
	v_med3_f32 v160, v32, v212, v213
	s_nop 0
	v_med3_f32 v48, v48, v214, v215
	v_add_f32 v32, v0, v16
	v_add_f32 v161, v160, v48
	v_add_f32 v32, v32, v161
	v_med3_f32 v49, v49, v214, v215
	v_bfe_u32 v0, v32, 20, 11
	v_med3_u32 v0, v0, s91, v190
	v_sub_u32_e32 v16, 0x40f, v0
	v_add_u32_e32 v0, 0xfffffdd0, v0
	v_cmp_gt_i32_e32 vcc, 0, v32
	v_mov_b32_e32 v48, s7
	s_nop 0
	v_cndmask_b32_e32 v0, v0, v16, vcc
	v_med3_f32 v16, v17, v209, v210
	v_med3_f32 v17, v33, v212, v213
	v_add_f32 v33, v1, v16
	v_add_f32 v160, v17, v49
	v_add_f32 v33, v33, v160
	v_cmp_eq_f32_e32 vcc, 0, v32
	v_bfe_u32 v1, v33, 20, 11
	v_med3_u32 v1, v1, s91, v190
	v_cndmask_b32_e32 v0, v0, v48, vcc
	v_sub_u32_e32 v16, 0x40f, v1
	v_add_u32_e32 v1, 0xfffffdd0, v1
	v_cmp_gt_i32_e64 s[98:99], 0, v33
	v_cmp_eq_f32_e32 vcc, 0, v33
	v_med3_f32 v49, v50, v214, v215
	v_cndmask_b32_e64 v1, v1, v16, s[98:99]
	v_cndmask_b32_e32 v16, v1, v48, vcc
	v_med3_f32 v1, v2, v207, v208
	v_med3_f32 v2, v18, v209, v210
	v_med3_f32 v18, v34, v212, v213
	v_add_f32 v34, v1, v2
	v_add_f32 v50, v18, v49
	v_add_f32 v34, v34, v50
	s_waitcnt lgkmcnt(0)
	v_cmp_eq_u32_e32 vcc, v16, v222
	v_bfe_u32 v1, v34, 20, 11
	v_med3_u32 v1, v1, s91, v190
	v_cndmask_b32_e64 v17, 0, 2, vcc
	v_sub_u32_e32 v2, 0x40f, v1
	v_add_u32_e32 v1, 0xfffffdd0, v1
	v_cmp_gt_i32_e64 s[98:99], 0, v34
	v_cmp_eq_f32_e32 vcc, 0, v34
	v_med3_f32 v18, v35, v212, v213
	v_cndmask_b32_e64 v1, v1, v2, s[98:99]
	v_med3_f32 v2, v3, v207, v208
	v_med3_f32 v3, v19, v209, v210
	v_cndmask_b32_e32 v1, v1, v48, vcc
	v_med3_f32 v19, v51, v214, v215
	v_add_f32 v35, v2, v3
	v_add_f32 v50, v18, v19
	v_add_f32 v35, v35, v50
	v_cmp_eq_u32_e32 vcc, v1, v222
	v_bfe_u32 v2, v35, 20, 11
	v_med3_u32 v2, v2, s91, v190
	v_cndmask_b32_e64 v49, 0, 4, vcc
	v_sub_u32_e32 v3, 0x40f, v2
	v_add_u32_e32 v2, 0xfffffdd0, v2
	v_cmp_gt_i32_e64 s[98:99], 0, v35
	v_cmp_eq_f32_e32 vcc, 0, v35
	v_med3_f32 v19, v36, v212, v213
	v_cndmask_b32_e64 v2, v2, v3, s[98:99]
	v_med3_f32 v3, v4, v207, v208
	v_med3_f32 v4, v20, v209, v210
	v_cndmask_b32_e32 v2, v2, v48, vcc
	v_med3_f32 v20, v52, v214, v215
	v_add_f32 v18, v3, v4
	v_add_f32 v36, v19, v20
	v_add_f32 v18, v18, v36
	v_cmp_eq_u32_e32 vcc, v2, v222
	v_bfe_u32 v3, v18, 20, 11
	v_med3_u32 v3, v3, s91, v190
	v_cndmask_b32_e64 v50, 0, 8, vcc
	v_sub_u32_e32 v4, 0x40f, v3
	v_add_u32_e32 v3, 0xfffffdd0, v3
	v_cmp_gt_i32_e64 s[98:99], 0, v18
	v_cmp_eq_f32_e32 vcc, 0, v18
	v_med3_f32 v20, v37, v212, v213
	v_cndmask_b32_e64 v3, v3, v4, s[98:99]
	v_med3_f32 v4, v5, v207, v208
	v_med3_f32 v5, v21, v209, v210
	v_cndmask_b32_e32 v3, v3, v48, vcc
	v_med3_f32 v21, v53, v214, v215
	v_add_f32 v19, v4, v5
	v_add_f32 v37, v20, v21
	v_add_f32 v19, v19, v37
	v_cmp_eq_u32_e32 vcc, v3, v222
	v_bfe_u32 v4, v19, 20, 11
	v_med3_u32 v4, v4, s91, v190
	v_cndmask_b32_e32 v36, 0, v186, vcc
	v_sub_u32_e32 v5, 0x40f, v4
	v_add_u32_e32 v4, 0xfffffdd0, v4
	v_cmp_gt_i32_e64 s[98:99], 0, v19
	v_cmp_eq_f32_e32 vcc, 0, v19
	v_med3_f32 v21, v38, v212, v213
	v_cndmask_b32_e64 v4, v4, v5, s[98:99]
	v_med3_f32 v5, v6, v207, v208
	v_med3_f32 v6, v22, v209, v210
	v_cndmask_b32_e32 v4, v4, v48, vcc
	v_med3_f32 v22, v54, v214, v215
	v_add_f32 v20, v5, v6
	v_add_f32 v38, v21, v22
	v_add_f32 v20, v20, v38
	v_cmp_eq_u32_e32 vcc, v4, v222
	v_bfe_u32 v5, v20, 20, 11
	v_med3_u32 v5, v5, s91, v190
	v_cndmask_b32_e32 v37, 0, v193, vcc
	v_sub_u32_e32 v6, 0x40f, v5
	v_add_u32_e32 v5, 0xfffffdd0, v5
	v_cmp_gt_i32_e64 s[98:99], 0, v20
	v_cmp_eq_f32_e32 vcc, 0, v20
	v_med3_f32 v22, v39, v212, v213
	v_cndmask_b32_e64 v5, v5, v6, s[98:99]
	v_med3_f32 v6, v7, v207, v208
	v_med3_f32 v7, v23, v209, v210
	v_cndmask_b32_e32 v5, v5, v48, vcc
	v_med3_f32 v23, v55, v214, v215
	v_add_f32 v21, v6, v7
	v_add_f32 v39, v22, v23
	v_add_f32 v21, v21, v39
	v_cmp_eq_u32_e32 vcc, v5, v222
	v_bfe_u32 v6, v21, 20, 11
; #define LAS __attribute__((address_space(3)))
; __device__ __forceinline__ int crow(int reg, int h) { return (reg & 3) + 8 * (reg >> 2) + 4 * h; }
; template <int STAGE>
; __device__ __forceinline__ void pass2(LAS unsigned char* lds, const bf16* kbase, int g, int t0, const bf16x8 (&qf)[4][4], const f32x4 lo4, const f32x4 hi4, int wave, int r, int h2) {
;     ...
;         for (int rg = 0; rg < 16; ++rg) {
;             const int c0 = att::crow(rg, 0);
;             float sv = fsum4_s(__builtin_amdgcn_fmed3f(acc[0][rg], lo4.x, hi4.x), __builtin_amdgcn_fmed3f(acc[1][rg], lo4.y, hi4.y),
;                                __builtin_amdgcn_fmed3f(acc[2][rg], lo4.z, hi4.z), __builtin_amdgcn_fmed3f(acc[3][rg], lo4.w, hi4.w));
;             const int b = bin2(sv, zi);
;             const bool valid = !DIAG || c0 <= lim;
;             if (STAGE == 0) {
;                 atomicAdd((unsigned*)&hist[r * HROW2 + (valid ? b : NB2)], 1u);
;             } else {
;                 if (valid && b > tb) gtw |= 1u << c0;
;                 if (valid && b == tb) eqw |= 1u << c0;
;                 svq[rg] = sv;
;             }
;         }
;         if (STAGE == 1) {
;             LAS unsigned char* st = lds + OFF2_SV + wave * 4096 + (r + 32 * h2) * 16;
; #pragma unroll
;             for (int q = 0; q < 4; ++q) *(LAS f32x4*)(st + q * 1024) = (f32x4){svq[4 * q], svq[4 * q + 1], svq[4 * q + 2], svq[4 * q + 3]};
	v_med3_u32 v6, v6, s91, v190
	v_cndmask_b32_e32 v38, 0, v194, vcc
	v_sub_u32_e32 v7, 0x40f, v6
	v_add_u32_e32 v6, 0xfffffdd0, v6
	v_cmp_gt_i32_e64 s[98:99], 0, v21
	v_cmp_eq_f32_e32 vcc, 0, v21
	v_med3_f32 v23, v40, v212, v213
	v_cndmask_b32_e64 v6, v6, v7, s[98:99]
	v_med3_f32 v7, v8, v207, v208
	v_med3_f32 v8, v24, v209, v210
	v_cndmask_b32_e32 v6, v6, v48, vcc
	v_med3_f32 v24, v56, v214, v215
	v_add_f32 v22, v7, v8
	v_add_f32 v40, v23, v24
	v_add_f32 v22, v22, v40
	v_cmp_eq_u32_e32 vcc, v6, v222
	v_bfe_u32 v7, v22, 20, 11
	v_med3_u32 v7, v7, s91, v190
	v_cndmask_b32_e32 v39, 0, v195, vcc
	v_sub_u32_e32 v8, 0x40f, v7
	v_add_u32_e32 v7, 0xfffffdd0, v7
	v_cmp_gt_i32_e64 s[98:99], 0, v22
	v_cmp_eq_f32_e32 vcc, 0, v22
	v_med3_f32 v24, v41, v212, v213
	v_cndmask_b32_e64 v7, v7, v8, s[98:99]
	v_med3_f32 v8, v9, v207, v208
	v_med3_f32 v9, v25, v209, v210
	v_cndmask_b32_e32 v7, v7, v48, vcc
	v_med3_f32 v25, v57, v214, v215
	v_add_f32 v23, v8, v9
	v_add_f32 v41, v24, v25
	v_add_f32 v23, v23, v41
	v_cmp_eq_u32_e32 vcc, v7, v222
	v_bfe_u32 v8, v23, 20, 11
	v_med3_u32 v8, v8, s91, v190
	v_cndmask_b32_e32 v40, 0, v196, vcc
	v_sub_u32_e32 v9, 0x40f, v8
	v_add_u32_e32 v8, 0xfffffdd0, v8
	v_cmp_gt_i32_e64 s[98:99], 0, v23
	v_cmp_eq_f32_e32 vcc, 0, v23
	v_med3_f32 v25, v42, v212, v213
	v_cndmask_b32_e64 v8, v8, v9, s[98:99]
	v_med3_f32 v9, v10, v207, v208
	v_med3_f32 v10, v26, v209, v210
	v_cndmask_b32_e32 v8, v8, v48, vcc
	v_med3_f32 v26, v58, v214, v215
	v_add_f32 v24, v9, v10
	v_add_f32 v42, v25, v26
	v_add_f32 v24, v24, v42
	v_cmp_eq_u32_e32 vcc, v8, v222
	v_bfe_u32 v9, v24, 20, 11
	v_med3_u32 v9, v9, s91, v190
	v_cndmask_b32_e32 v41, 0, v197, vcc
	v_sub_u32_e32 v10, 0x40f, v9
	v_add_u32_e32 v9, 0xfffffdd0, v9
	v_cmp_gt_i32_e64 s[98:99], 0, v24
	v_cmp_eq_f32_e32 vcc, 0, v24
	v_med3_f32 v26, v43, v212, v213
	v_cndmask_b32_e64 v9, v9, v10, s[98:99]
	v_med3_f32 v10, v11, v207, v208
	v_med3_f32 v11, v27, v209, v210
	v_cndmask_b32_e32 v9, v9, v48, vcc
	v_med3_f32 v27, v59, v214, v215
	v_add_f32 v25, v10, v11
	v_add_f32 v43, v26, v27
	v_add_f32 v25, v25, v43
	v_cmp_eq_u32_e32 vcc, v9, v222
	v_bfe_u32 v10, v25, 20, 11
	v_med3_u32 v10, v10, s91, v190
	v_cndmask_b32_e32 v42, 0, v198, vcc
	v_sub_u32_e32 v11, 0x40f, v10
	v_add_u32_e32 v10, 0xfffffdd0, v10
	v_cmp_gt_i32_e64 s[98:99], 0, v25
	v_cmp_eq_f32_e32 vcc, 0, v25
	v_med3_f32 v27, v44, v212, v213
	v_cndmask_b32_e64 v10, v10, v11, s[98:99]
	v_med3_f32 v11, v12, v207, v208
	v_med3_f32 v12, v28, v209, v210
	v_cndmask_b32_e32 v10, v10, v48, vcc
	v_med3_f32 v28, v60, v214, v215
	v_add_f32 v26, v11, v12
	v_add_f32 v44, v27, v28
	v_add_f32 v26, v26, v44
	v_cmp_eq_u32_e32 vcc, v10, v222
	v_bfe_u32 v11, v26, 20, 11
	v_med3_u32 v11, v11, s91, v190
	v_cndmask_b32_e32 v43, 0, v199, vcc
	v_sub_u32_e32 v12, 0x40f, v11
	v_add_u32_e32 v11, 0xfffffdd0, v11
	v_cmp_gt_i32_e64 s[98:99], 0, v26
	v_cmp_eq_f32_e32 vcc, 0, v26
	v_med3_f32 v28, v45, v212, v213
	v_cndmask_b32_e64 v11, v11, v12, s[98:99]
	v_med3_f32 v12, v13, v207, v208
	v_med3_f32 v13, v29, v209, v210
	v_cndmask_b32_e32 v11, v11, v48, vcc
	v_med3_f32 v29, v61, v214, v215
	v_add_f32 v27, v12, v13
	v_add_f32 v45, v28, v29
	v_add_f32 v27, v27, v45
	v_cmp_eq_u32_e32 vcc, v11, v222
	v_bfe_u32 v12, v27, 20, 11
	v_med3_u32 v12, v12, s91, v190
	v_cndmask_b32_e32 v44, 0, v200, vcc
	v_sub_u32_e32 v13, 0x40f, v12
	v_add_u32_e32 v12, 0xfffffdd0, v12
	v_cmp_gt_i32_e64 s[98:99], 0, v27
	v_cmp_eq_f32_e32 vcc, 0, v27
	v_med3_f32 v29, v46, v212, v213
	v_cndmask_b32_e64 v12, v12, v13, s[98:99]
	v_med3_f32 v13, v14, v207, v208
	v_med3_f32 v14, v30, v209, v210
	v_cndmask_b32_e32 v12, v12, v48, vcc
	v_med3_f32 v30, v62, v214, v215
	v_add_f32 v28, v13, v14
	v_add_f32 v46, v29, v30
	v_add_f32 v28, v28, v46
	v_cmp_eq_u32_e32 vcc, v12, v222
	v_bfe_u32 v13, v28, 20, 11
	v_med3_u32 v13, v13, s91, v190
	v_cndmask_b32_e32 v45, 0, v201, vcc
	v_sub_u32_e32 v14, 0x40f, v13
	v_add_u32_e32 v13, 0xfffffdd0, v13
	v_cmp_gt_i32_e64 s[98:99], 0, v28
	v_cmp_eq_f32_e32 vcc, 0, v28
	v_med3_f32 v46, v63, v214, v215
	v_cndmask_b32_e64 v13, v13, v14, s[98:99]
	v_med3_f32 v14, v15, v207, v208
	v_med3_f32 v15, v31, v209, v210
	v_cndmask_b32_e32 v13, v13, v48, vcc
	v_med3_f32 v31, v47, v212, v213
	v_add_f32 v29, v14, v15
	v_add_f32 v47, v31, v46
	v_add_f32 v29, v29, v47
	v_cmp_eq_u32_e32 vcc, v13, v222
	v_bfe_u32 v14, v29, 20, 11
	v_med3_u32 v14, v14, s91, v190
	v_cndmask_b32_e32 v30, 0, v202, vcc
	v_sub_u32_e32 v15, 0x40f, v14
	v_add_u32_e32 v14, 0xfffffdd0, v14
	v_cmp_gt_i32_e64 s[98:99], 0, v29
	v_cmp_eq_f32_e32 vcc, 0, v29
	ds_write_b128 v223, v[32:35]
	ds_write_b128 v223, v[18:21] offset:1024
	ds_write_b128 v223, v[22:25] offset:2048
	ds_write_b128 v223, v[26:29] offset:3072
	v_cndmask_b32_e64 v14, v14, v15, s[98:99]
	v_cndmask_b32_e32 v14, v14, v48, vcc
	v_cmp_eq_u32_e32 vcc, v14, v222
	s_nop 1
	v_cndmask_b32_e32 v15, 0, v203, vcc
	v_cmp_eq_u32_e32 vcc, v0, v222
	s_nop 1
	v_cndmask_b32_e64 v18, 0, 1, vcc
	v_or_b32_e32 v17, v17, v18
	v_or3_b32 v17, v17, v49, v50
	v_or3_b32 v17, v17, v36, v37
	v_or3_b32 v17, v17, v38, v39
	v_or3_b32 v17, v17, v40, v41
	v_or3_b32 v17, v17, v42, v43
	v_or3_b32 v17, v17, v44, v45
	v_or3_b32 v17, v17, v30, v15
	v_add_u32_e32 v15, s6, v219
	s_branch .LBB0_830

; #define LAS __attribute__((address_space(3)))
; template <int STAGE>
; __device__ __forceinline__ void pass2(LAS unsigned char* lds, const bf16* kbase, int g, int t0, const bf16x8 (&qf)[4][4], const f32x4 lo4, const f32x4 hi4, int wave, int r, int h2) {
;     ...
;         for (int hd = 0; hd < 4; ++hd) {
;             acc[hd] = f32x16{};
; #pragma unroll
;             for (int s = 0; s < 4; ++s) acc[hd] = __builtin_amdgcn_mfma_f32_32x32x16_bf16(WN ? kn[s] : kf[s], qf[hd][s], acc[hd], 0, 0, 0);
;         }
;         const int zi = (8191 - 32 * kt) >> 7;
;         const int lim = tq - 32 * kt - 4 * h2;
;         unsigned gtw = 0u, eqw = 0u;
;         float svq[16];
; #pragma unroll
;         for (int rg = 0; rg < 16; ++rg) {
;             const int c0 = att::crow(rg, 0);
;             float sv = fsum4_s(__builtin_amdgcn_fmed3f(acc[0][rg], lo4.x, hi4.x), __builtin_amdgcn_fmed3f(acc[1][rg], lo4.y, hi4.y),
;                                __builtin_amdgcn_fmed3f(acc[2][rg], lo4.z, hi4.z), __builtin_amdgcn_fmed3f(acc[3][rg], lo4.w, hi4.w));
;             const int b = bin2(sv, zi);
;             const bool valid = !DIAG || c0 <= lim;
;             if (STAGE == 0) {
;     ...
;                 if (valid && b > tb) gtw |= 1u << c0;
;                 if (valid && b == tb) eqw |= 1u << c0;
;                 svq[rg] = sv;
;             }
;         }
;         if (STAGE == 1) {
;             LAS unsigned char* st = lds + OFF2_SV + wave * 4096 + (r + 32 * h2) * 16;
; #pragma unroll
;             for (int q = 0; q < 4; ++q) *(LAS f32x4*)(st + q * 1024) = (f32x4){svq[4 * q], svq[4 * q + 1], svq[4 * q + 2], svq[4 * q + 3]};
;             unsigned e = eqw;
;             while (__any(e != 0u)) {
;                 if (e != 0u) {
;                     const int c = __builtin_ctz(e); e &= e - 1u;
;                     float svv = *(const LAS float*)(st + (c >> 3) * 1024 + (c & 3) * 4);
;                     svv = fadd_s(svv, 0.0f);
;                     const unsigned pos = atomicAdd((unsigned*)&cntp[r], 1u);
;                     if (pos < (unsigned)CAP2) cand[r * CAP2 + pos] = ((unsigned long long)okey(svv) << 13) | (unsigned long long)(8191 - (32 * kt + c + 4 * h2));
;                 }
;             }
;             gtw <<= 4 * h2;
;             { auto rr = __builtin_amdgcn_permlane32_swap(gtw, gtw, false, false); gtw = rr[0] | rr[1]; }
;             if (h2 == 0) gtm[r * HROW + kt] = gtw;
.LBB0_834:
.LBB0_835:
	v_cmp_gt_i32_e32 vcc, v16, v222
	v_cmp_gt_i32_e64 s[98:99], v1, v222
	v_cmp_gt_i32_e64 s[100:101], v2, v222
	v_cndmask_b32_e64 v15, 0, 2, vcc
	v_cmp_gt_i32_e32 vcc, v3, v222
	v_cndmask_b32_e64 v1, 0, 4, s[98:99]
	v_cmp_gt_i32_e64 s[98:99], v4, v222
	v_cndmask_b32_e64 v2, 0, 8, s[100:101]
	v_cmp_gt_i32_e64 s[100:101], v5, v222
	v_cndmask_b32_e64 v3, 0, v186, vcc
	v_cmp_gt_i32_e32 vcc, v6, v222
	v_cndmask_b32_e64 v4, 0, v193, s[98:99]
	v_cmp_gt_i32_e64 s[98:99], v7, v222
	v_cndmask_b32_e64 v5, 0, v194, s[100:101]
	v_cmp_gt_i32_e64 s[100:101], v8, v222
	v_cndmask_b32_e64 v6, 0, v195, vcc
	v_cmp_gt_i32_e32 vcc, v9, v222
	v_cndmask_b32_e64 v7, 0, v196, s[98:99]
	v_cmp_gt_i32_e64 s[98:99], v10, v222
	v_cndmask_b32_e64 v8, 0, v197, s[100:101]
	v_cmp_gt_i32_e64 s[100:101], v11, v222
	v_cndmask_b32_e64 v9, 0, v198, vcc
	v_cmp_gt_i32_e32 vcc, v12, v222
	v_cndmask_b32_e64 v10, 0, v199, s[98:99]
	v_cmp_gt_i32_e64 s[98:99], v13, v222
	v_cndmask_b32_e64 v11, 0, v200, s[100:101]
	v_cmp_gt_i32_e64 s[100:101], v14, v222
	v_cndmask_b32_e64 v12, 0, v201, vcc
	v_cmp_gt_i32_e32 vcc, v0, v222
	v_cndmask_b32_e64 v13, 0, v202, s[98:99]
	v_cndmask_b32_e64 v14, 0, v203, s[100:101]
	v_cndmask_b32_e64 v0, 0, 1, vcc
	v_or_b32_e32 v0, v15, v0
	v_or3_b32 v0, v0, v1, v2
	v_or3_b32 v0, v0, v3, v4
	v_or3_b32 v0, v0, v5, v6
	v_or3_b32 v0, v0, v7, v8
	v_or3_b32 v0, v0, v9, v10
	v_or3_b32 v0, v0, v11, v12
	v_or3_b32 v0, v0, v13, v14
	v_lshlrev_b32_e32 v0, v219, v0
	v_mov_b32_e32 v1, v0
	s_nop 1
	v_permlane32_swap_b32_e32 v0, v1
	s_and_saveexec_b64 s[6:7], s[84:85]
	v_or_b32_e32 v0, v0, v1
	v_lshl_add_u32 v1, s0, 2, v217
	ds_write_b32 v1, v0
	s_or_b64 exec, exec, s[6:7]
	s_mov_b64 s[6:7], -1
	s_andn2_b64 vcc, exec, s[4:5]
	s_mov_b64 s[4:5], -1
	s_cbranch_vccnz .LBB0_854
	s_add_i32 s10, s0, 16
	s_cmp_gt_u32 s10, s64
	s_cselect_b64 s[4:5], -1, 0
	v_mov_b64_e32 v[174:175], v[130:131]
	v_mov_b64_e32 v[170:171], v[134:135]
	v_mov_b64_e32 v[166:167], v[138:139]
	v_mov_b64_e32 v[162:163], v[142:143]
	s_and_b64 vcc, exec, s[4:5]
	v_mov_b64_e32 v[172:173], v[128:129]
	v_mov_b64_e32 v[168:169], v[132:133]
	v_mov_b64_e32 v[164:165], v[136:137]
	v_mov_b64_e32 v[160:161], v[140:141]
	s_cbranch_vccnz .LBB0_840
	s_lshl_b32 s6, s10, 5
	v_mad_u64_u32 v[0:1], s[6:7], s6, v187, v[178:179]
	global_load_dwordx4 v[160:163], v[0:1], off
	global_load_dwordx4 v[164:167], v[0:1], off offset:32
	global_load_dwordx4 v[168:171], v[0:1], off offset:64
	global_load_dwordx4 v[172:175], v[0:1], off offset:96
.LBB0_840:
	s_cmp_lg_u32 s1, s64
	s_cbranch_scc0 .LBB0_853
	v_mfma_f32_32x32x16_bf16 v[0:15], v[156:159], v[64:67], 0
	s_lshl_b32 s1, s1, 5
	s_sub_i32 s6, 0x1fe0, s1
	s_lshr_b32 s6, s6, 7
	s_addk_i32 s6, 0xd0
	v_mfma_f32_32x32x16_bf16 v[16:31], v[156:159], v[80:83], 0
	v_mfma_f32_32x32x16_bf16 v[32:47], v[156:159], v[96:99], 0
	v_mfma_f32_32x32x16_bf16 v[48:63], v[156:159], v[112:115], 0
	v_mfma_f32_32x32x16_bf16 v[0:15], v[152:155], v[68:71], v[0:15]
	v_mfma_f32_32x32x16_bf16 v[16:31], v[152:155], v[84:87], v[16:31]
	v_mfma_f32_32x32x16_bf16 v[32:47], v[152:155], v[100:103], v[32:47]
	v_mfma_f32_32x32x16_bf16 v[48:63], v[152:155], v[116:119], v[48:63]
	v_mfma_f32_32x32x16_bf16 v[0:15], v[148:151], v[72:75], v[0:15]
	v_mfma_f32_32x32x16_bf16 v[16:31], v[148:151], v[88:91], v[16:31]
	v_mfma_f32_32x32x16_bf16 v[32:47], v[148:151], v[104:107], v[32:47]
	v_mfma_f32_32x32x16_bf16 v[48:63], v[148:151], v[120:123], v[48:63]
	v_mfma_f32_32x32x16_bf16 v[0:15], v[144:147], v[76:79], v[0:15]
	v_mfma_f32_32x32x16_bf16 v[16:31], v[144:147], v[92:95], v[16:31]
	s_nop 10
	v_med3_f32 v0, v0, v207, v208
	v_med3_f32 v1, v1, v207, v208
	v_mfma_f32_32x32x16_bf16 v[32:47], v[144:147], v[108:111], v[32:47]
	v_med3_f32 v16, v16, v209, v210
	v_mfma_f32_32x32x16_bf16 v[48:63], v[144:147], v[124:127], v[48:63]
	s_nop 9
	v_med3_f32 v176, v32, v212, v213
	s_nop 0
	v_med3_f32 v48, v48, v214, v215
	v_add_f32 v32, v0, v16
	v_add_f32 v218, v176, v48
	v_add_f32 v32, v32, v218
	v_med3_f32 v49, v49, v214, v215
	v_bfe_u32 v0, v32, 20, 11
	v_med3_u32 v0, v0, s91, v190
	v_sub_u32_e32 v16, 0x40f, v0
	v_add_u32_e32 v0, 0xfffffdd0, v0
	v_cmp_gt_i32_e32 vcc, 0, v32
	v_mov_b32_e32 v48, s6
	s_nop 0
	v_cndmask_b32_e32 v0, v0, v16, vcc
	v_med3_f32 v16, v17, v209, v210
	v_med3_f32 v17, v33, v212, v213
	v_add_f32 v33, v1, v16
	v_add_f32 v176, v17, v49
	v_add_f32 v33, v33, v176
	v_cmp_eq_f32_e32 vcc, 0, v32
	v_bfe_u32 v1, v33, 20, 11
	v_med3_u32 v1, v1, s91, v190
	v_cndmask_b32_e32 v0, v0, v48, vcc
	v_sub_u32_e32 v16, 0x40f, v1
	v_add_u32_e32 v1, 0xfffffdd0, v1
	v_cmp_gt_i32_e64 s[98:99], 0, v33
	v_cmp_eq_f32_e32 vcc, 0, v33
	v_med3_f32 v49, v50, v214, v215
	v_cndmask_b32_e64 v1, v1, v16, s[98:99]
	v_cndmask_b32_e32 v16, v1, v48, vcc
	v_med3_f32 v1, v2, v207, v208
	v_med3_f32 v2, v18, v209, v210
	v_med3_f32 v18, v34, v212, v213
	v_add_f32 v34, v1, v2
	v_add_f32 v50, v18, v49
	v_add_f32 v34, v34, v50
	v_cmp_eq_u32_e32 vcc, v16, v222
	v_bfe_u32 v1, v34, 20, 11
	v_med3_u32 v1, v1, s91, v190
	v_cndmask_b32_e64 v17, 0, 2, vcc
	v_sub_u32_e32 v2, 0x40f, v1
	v_add_u32_e32 v1, 0xfffffdd0, v1
	v_cmp_gt_i32_e64 s[98:99], 0, v34
	v_cmp_eq_f32_e32 vcc, 0, v34
	v_med3_f32 v18, v35, v212, v213
	v_cndmask_b32_e64 v1, v1, v2, s[98:99]
	v_med3_f32 v2, v3, v207, v208
	v_med3_f32 v3, v19, v209, v210
	v_cndmask_b32_e32 v1, v1, v48, vcc
	v_med3_f32 v19, v51, v214, v215
	v_add_f32 v35, v2, v3
	v_add_f32 v50, v18, v19
	v_add_f32 v35, v35, v50
	v_cmp_eq_u32_e32 vcc, v1, v222
	v_bfe_u32 v2, v35, 20, 11
	v_med3_u32 v2, v2, s91, v190
	v_cndmask_b32_e64 v49, 0, 4, vcc
	v_sub_u32_e32 v3, 0x40f, v2
	v_add_u32_e32 v2, 0xfffffdd0, v2
	v_cmp_gt_i32_e64 s[98:99], 0, v35
; __device__ __forceinline__ int crow(int reg, int h) { return (reg & 3) + 8 * (reg >> 2) + 4 * h; }
; template <int STAGE>
; __device__ __forceinline__ void pass2(LAS unsigned char* lds, const bf16* kbase, int g, int t0, const bf16x8 (&qf)[4][4], const f32x4 lo4, const f32x4 hi4, int wave, int r, int h2) {
;     ...
;         for (int rg = 0; rg < 16; ++rg) {
;             const int c0 = att::crow(rg, 0);
;             float sv = fsum4_s(__builtin_amdgcn_fmed3f(acc[0][rg], lo4.x, hi4.x), __builtin_amdgcn_fmed3f(acc[1][rg], lo4.y, hi4.y),
;                                __builtin_amdgcn_fmed3f(acc[2][rg], lo4.z, hi4.z), __builtin_amdgcn_fmed3f(acc[3][rg], lo4.w, hi4.w));
;             const int b = bin2(sv, zi);
;             const bool valid = !DIAG || c0 <= lim;
;             if (STAGE == 0) {
;                 atomicAdd((unsigned*)&hist[r * HROW2 + (valid ? b : NB2)], 1u);
;             } else {
;                 if (valid && b > tb) gtw |= 1u << c0;
;                 if (valid && b == tb) eqw |= 1u << c0;
;                 svq[rg] = sv;
	v_cmp_eq_f32_e32 vcc, 0, v35
	v_med3_f32 v19, v36, v212, v213
	v_cndmask_b32_e64 v2, v2, v3, s[98:99]
	v_med3_f32 v3, v4, v207, v208
	v_med3_f32 v4, v20, v209, v210
	v_cndmask_b32_e32 v2, v2, v48, vcc
	v_med3_f32 v20, v52, v214, v215
	v_add_f32 v18, v3, v4
	v_add_f32 v36, v19, v20
	v_add_f32 v18, v18, v36
	v_cmp_eq_u32_e32 vcc, v2, v222
	v_bfe_u32 v3, v18, 20, 11
	v_med3_u32 v3, v3, s91, v190
	v_cndmask_b32_e64 v50, 0, 8, vcc
	v_sub_u32_e32 v4, 0x40f, v3
	v_add_u32_e32 v3, 0xfffffdd0, v3
	v_cmp_gt_i32_e64 s[98:99], 0, v18
	v_cmp_eq_f32_e32 vcc, 0, v18
	v_med3_f32 v20, v37, v212, v213
	v_cndmask_b32_e64 v3, v3, v4, s[98:99]
	v_med3_f32 v4, v5, v207, v208
	v_med3_f32 v5, v21, v209, v210
	v_cndmask_b32_e32 v3, v3, v48, vcc
	v_med3_f32 v21, v53, v214, v215
	v_add_f32 v19, v4, v5
	v_add_f32 v37, v20, v21
	v_add_f32 v19, v19, v37
	v_cmp_eq_u32_e32 vcc, v3, v222
	v_bfe_u32 v4, v19, 20, 11
	v_med3_u32 v4, v4, s91, v190
	v_cndmask_b32_e32 v36, 0, v186, vcc
	v_sub_u32_e32 v5, 0x40f, v4
	v_add_u32_e32 v4, 0xfffffdd0, v4
	v_cmp_gt_i32_e64 s[98:99], 0, v19
	v_cmp_eq_f32_e32 vcc, 0, v19
	v_med3_f32 v21, v38, v212, v213
	v_cndmask_b32_e64 v4, v4, v5, s[98:99]
	v_med3_f32 v5, v6, v207, v208
	v_med3_f32 v6, v22, v209, v210
	v_cndmask_b32_e32 v4, v4, v48, vcc
	v_med3_f32 v22, v54, v214, v215
	v_add_f32 v20, v5, v6
	v_add_f32 v38, v21, v22
	v_add_f32 v20, v20, v38
	v_cmp_eq_u32_e32 vcc, v4, v222
	v_bfe_u32 v5, v20, 20, 11
	v_med3_u32 v5, v5, s91, v190
	v_cndmask_b32_e32 v37, 0, v193, vcc
	v_sub_u32_e32 v6, 0x40f, v5
	v_add_u32_e32 v5, 0xfffffdd0, v5
	v_cmp_gt_i32_e64 s[98:99], 0, v20
	v_cmp_eq_f32_e32 vcc, 0, v20
	v_med3_f32 v22, v39, v212, v213
	v_cndmask_b32_e64 v5, v5, v6, s[98:99]
	v_med3_f32 v6, v7, v207, v208
	v_med3_f32 v7, v23, v209, v210
	v_cndmask_b32_e32 v5, v5, v48, vcc
	v_med3_f32 v23, v55, v214, v215
	v_add_f32 v21, v6, v7
	v_add_f32 v39, v22, v23
	v_add_f32 v21, v21, v39
	v_cmp_eq_u32_e32 vcc, v5, v222
	v_bfe_u32 v6, v21, 20, 11
	v_med3_u32 v6, v6, s91, v190
	v_cndmask_b32_e32 v38, 0, v194, vcc
	v_sub_u32_e32 v7, 0x40f, v6
	v_add_u32_e32 v6, 0xfffffdd0, v6
	v_cmp_gt_i32_e64 s[98:99], 0, v21
	v_cmp_eq_f32_e32 vcc, 0, v21
	v_med3_f32 v23, v40, v212, v213
	v_cndmask_b32_e64 v6, v6, v7, s[98:99]
	v_med3_f32 v7, v8, v207, v208
	v_med3_f32 v8, v24, v209, v210
	v_cndmask_b32_e32 v6, v6, v48, vcc
	v_med3_f32 v24, v56, v214, v215
	v_add_f32 v22, v7, v8
	v_add_f32 v40, v23, v24
	v_add_f32 v22, v22, v40
	v_cmp_eq_u32_e32 vcc, v6, v222
	v_bfe_u32 v7, v22, 20, 11
	v_med3_u32 v7, v7, s91, v190
	v_cndmask_b32_e32 v39, 0, v195, vcc
	v_sub_u32_e32 v8, 0x40f, v7
	v_add_u32_e32 v7, 0xfffffdd0, v7
	v_cmp_gt_i32_e64 s[98:99], 0, v22
	v_cmp_eq_f32_e32 vcc, 0, v22
	v_med3_f32 v24, v41, v212, v213
	v_cndmask_b32_e64 v7, v7, v8, s[98:99]
	v_med3_f32 v8, v9, v207, v208
	v_med3_f32 v9, v25, v209, v210
	v_cndmask_b32_e32 v7, v7, v48, vcc
	v_med3_f32 v25, v57, v214, v215
	v_add_f32 v23, v8, v9
	v_add_f32 v41, v24, v25
	v_add_f32 v23, v23, v41
	v_cmp_eq_u32_e32 vcc, v7, v222
	v_bfe_u32 v8, v23, 20, 11
	v_med3_u32 v8, v8, s91, v190
	v_cndmask_b32_e32 v40, 0, v196, vcc
	v_sub_u32_e32 v9, 0x40f, v8
	v_add_u32_e32 v8, 0xfffffdd0, v8
	v_cmp_gt_i32_e64 s[98:99], 0, v23
	v_cmp_eq_f32_e32 vcc, 0, v23
	v_med3_f32 v25, v42, v212, v213
	v_cndmask_b32_e64 v8, v8, v9, s[98:99]
	v_med3_f32 v9, v10, v207, v208
	v_med3_f32 v10, v26, v209, v210
	v_cndmask_b32_e32 v8, v8, v48, vcc
	v_med3_f32 v26, v58, v214, v215
	v_add_f32 v24, v9, v10
	v_add_f32 v42, v25, v26
	v_add_f32 v24, v24, v42
	v_cmp_eq_u32_e32 vcc, v8, v222
	v_bfe_u32 v9, v24, 20, 11
	v_med3_u32 v9, v9, s91, v190
; #define LAS __attribute__((address_space(3)))
; __device__ __forceinline__ int crow(int reg, int h) { return (reg & 3) + 8 * (reg >> 2) + 4 * h; }
; template <int STAGE>
; __device__ __forceinline__ void pass2(LAS unsigned char* lds, const bf16* kbase, int g, int t0, const bf16x8 (&qf)[4][4], const f32x4 lo4, const f32x4 hi4, int wave, int r, int h2) {
;     ...
;         for (int rg = 0; rg < 16; ++rg) {
;             const int c0 = att::crow(rg, 0);
;             float sv = fsum4_s(__builtin_amdgcn_fmed3f(acc[0][rg], lo4.x, hi4.x), __builtin_amdgcn_fmed3f(acc[1][rg], lo4.y, hi4.y),
;                                __builtin_amdgcn_fmed3f(acc[2][rg], lo4.z, hi4.z), __builtin_amdgcn_fmed3f(acc[3][rg], lo4.w, hi4.w));
;             const int b = bin2(sv, zi);
;             const bool valid = !DIAG || c0 <= lim;
;             if (STAGE == 0) {
;                 atomicAdd((unsigned*)&hist[r * HROW2 + (valid ? b : NB2)], 1u);
;             } else {
;                 if (valid && b > tb) gtw |= 1u << c0;
;                 if (valid && b == tb) eqw |= 1u << c0;
;                 svq[rg] = sv;
;             }
;         }
;         if (STAGE == 1) {
;             LAS unsigned char* st = lds + OFF2_SV + wave * 4096 + (r + 32 * h2) * 16;
; #pragma unroll
;             for (int q = 0; q < 4; ++q) *(LAS f32x4*)(st + q * 1024) = (f32x4){svq[4 * q], svq[4 * q + 1], svq[4 * q + 2], svq[4 * q + 3]};
	v_cndmask_b32_e32 v41, 0, v197, vcc
	v_sub_u32_e32 v10, 0x40f, v9
	v_add_u32_e32 v9, 0xfffffdd0, v9
	v_cmp_gt_i32_e64 s[98:99], 0, v24
	v_cmp_eq_f32_e32 vcc, 0, v24
	v_med3_f32 v26, v43, v212, v213
	v_cndmask_b32_e64 v9, v9, v10, s[98:99]
	v_med3_f32 v10, v11, v207, v208
	v_med3_f32 v11, v27, v209, v210
	v_cndmask_b32_e32 v9, v9, v48, vcc
	v_med3_f32 v27, v59, v214, v215
	v_add_f32 v25, v10, v11
	v_add_f32 v43, v26, v27
	v_add_f32 v25, v25, v43
	v_cmp_eq_u32_e32 vcc, v9, v222
	v_bfe_u32 v10, v25, 20, 11
	v_med3_u32 v10, v10, s91, v190
	v_cndmask_b32_e32 v42, 0, v198, vcc
	v_sub_u32_e32 v11, 0x40f, v10
	v_add_u32_e32 v10, 0xfffffdd0, v10
	v_cmp_gt_i32_e64 s[98:99], 0, v25
	v_cmp_eq_f32_e32 vcc, 0, v25
	v_med3_f32 v27, v44, v212, v213
	v_cndmask_b32_e64 v10, v10, v11, s[98:99]
	v_med3_f32 v11, v12, v207, v208
	v_med3_f32 v12, v28, v209, v210
	v_cndmask_b32_e32 v10, v10, v48, vcc
	v_med3_f32 v28, v60, v214, v215
	v_add_f32 v26, v11, v12
	v_add_f32 v44, v27, v28
	v_add_f32 v26, v26, v44
	v_cmp_eq_u32_e32 vcc, v10, v222
	v_bfe_u32 v11, v26, 20, 11
	v_med3_u32 v11, v11, s91, v190
	v_cndmask_b32_e32 v43, 0, v199, vcc
	v_sub_u32_e32 v12, 0x40f, v11
	v_add_u32_e32 v11, 0xfffffdd0, v11
	v_cmp_gt_i32_e64 s[98:99], 0, v26
	v_cmp_eq_f32_e32 vcc, 0, v26
	v_med3_f32 v28, v45, v212, v213
	v_cndmask_b32_e64 v11, v11, v12, s[98:99]
	v_med3_f32 v12, v13, v207, v208
	v_med3_f32 v13, v29, v209, v210
	v_cndmask_b32_e32 v11, v11, v48, vcc
	v_med3_f32 v29, v61, v214, v215
	v_add_f32 v27, v12, v13
	v_add_f32 v45, v28, v29
	v_add_f32 v27, v27, v45
	v_cmp_eq_u32_e32 vcc, v11, v222
	v_bfe_u32 v12, v27, 20, 11
	v_med3_u32 v12, v12, s91, v190
	v_cndmask_b32_e32 v44, 0, v200, vcc
	v_sub_u32_e32 v13, 0x40f, v12
	v_add_u32_e32 v12, 0xfffffdd0, v12
	v_cmp_gt_i32_e64 s[98:99], 0, v27
	v_cmp_eq_f32_e32 vcc, 0, v27
	v_med3_f32 v29, v46, v212, v213
	v_cndmask_b32_e64 v12, v12, v13, s[98:99]
	v_med3_f32 v13, v14, v207, v208
	v_med3_f32 v14, v30, v209, v210
	v_cndmask_b32_e32 v12, v12, v48, vcc
	v_med3_f32 v30, v62, v214, v215
	v_add_f32 v28, v13, v14
	v_add_f32 v46, v29, v30
	v_add_f32 v28, v28, v46
	v_cmp_eq_u32_e32 vcc, v12, v222
	v_bfe_u32 v13, v28, 20, 11
	v_med3_u32 v13, v13, s91, v190
	v_cndmask_b32_e32 v45, 0, v201, vcc
	v_sub_u32_e32 v14, 0x40f, v13
	v_add_u32_e32 v13, 0xfffffdd0, v13
	v_cmp_gt_i32_e64 s[98:99], 0, v28
	v_cmp_eq_f32_e32 vcc, 0, v28
	v_med3_f32 v46, v63, v214, v215
	v_cndmask_b32_e64 v13, v13, v14, s[98:99]
	v_med3_f32 v14, v15, v207, v208
	v_med3_f32 v15, v31, v209, v210
	v_cndmask_b32_e32 v13, v13, v48, vcc
	v_med3_f32 v31, v47, v212, v213
	v_add_f32 v29, v14, v15
	v_add_f32 v47, v31, v46
	v_add_f32 v29, v29, v47
	v_cmp_eq_u32_e32 vcc, v13, v222
	v_bfe_u32 v14, v29, 20, 11
	v_med3_u32 v14, v14, s91, v190
	v_cndmask_b32_e32 v30, 0, v202, vcc
	v_sub_u32_e32 v15, 0x40f, v14
	v_add_u32_e32 v14, 0xfffffdd0, v14
	v_cmp_gt_i32_e64 s[98:99], 0, v29
	v_cmp_eq_f32_e32 vcc, 0, v29
	ds_write_b128 v223, v[32:35]
	ds_write_b128 v223, v[18:21] offset:1024
	ds_write_b128 v223, v[22:25] offset:2048
	ds_write_b128 v223, v[26:29] offset:3072
	v_cndmask_b32_e64 v14, v14, v15, s[98:99]
	v_cndmask_b32_e32 v14, v14, v48, vcc
	v_cmp_eq_u32_e32 vcc, v14, v222
	s_nop 1
	v_cndmask_b32_e32 v15, 0, v203, vcc
	v_cmp_eq_u32_e32 vcc, v0, v222
	s_nop 1
	v_cndmask_b32_e64 v18, 0, 1, vcc
	v_or_b32_e32 v17, v17, v18
	v_or3_b32 v17, v17, v49, v50
	v_or3_b32 v17, v17, v36, v37
	v_or3_b32 v17, v17, v38, v39
	v_or3_b32 v17, v17, v40, v41
	v_or3_b32 v17, v17, v42, v43
	v_or3_b32 v17, v17, v44, v45
	v_or3_b32 v17, v17, v30, v15
	v_add_u32_e32 v15, s1, v219
	s_branch .LBB0_844

; #define LAS __attribute__((address_space(3)))
; __device__ __forceinline__ unsigned okey(float f) { const unsigned u = __float_as_uint(f); return (u & 0x80000000u) ? ~u : (u | 0x80000000u); }
; __device__ __forceinline__ float fadd_s(float a, float b) { float r; asm("v_add_f32 %0, %1, %2" : "=v"(r) : "v"(a), "v"(b)); return r; }
; template <int STAGE>
; __device__ __forceinline__ void pass2(LAS unsigned char* lds, const bf16* kbase, int g, int t0, const bf16x8 (&qf)[4][4], const f32x4 lo4, const f32x4 hi4, int wave, int r, int h2) {
;     ...
;                 if (valid && b > tb) gtw |= 1u << c0;
;                 if (valid && b == tb) eqw |= 1u << c0;
;                 svq[rg] = sv;
;             }
;         }
;         if (STAGE == 1) {
;             LAS unsigned char* st = lds + OFF2_SV + wave * 4096 + (r + 32 * h2) * 16;
; #pragma unroll
;             for (int q = 0; q < 4; ++q) *(LAS f32x4*)(st + q * 1024) = (f32x4){svq[4 * q], svq[4 * q + 1], svq[4 * q + 2], svq[4 * q + 3]};
;             unsigned e = eqw;
;             while (__any(e != 0u)) {
;                 if (e != 0u) {
;                     const int c = __builtin_ctz(e); e &= e - 1u;
;                     float svv = *(const LAS float*)(st + (c >> 3) * 1024 + (c & 3) * 4);
;                     svv = fadd_s(svv, 0.0f);
;                     const unsigned pos = atomicAdd((unsigned*)&cntp[r], 1u);
;                     if (pos < (unsigned)CAP2) cand[r * CAP2 + pos] = ((unsigned long long)okey(svv) << 13) | (unsigned long long)(8191 - (32 * kt + c + 4 * h2));
;                 }
;             }
;             gtw <<= 4 * h2;
;             { auto rr = __builtin_amdgcn_permlane32_swap(gtw, gtw, false, false); gtw = rr[0] | rr[1]; }
;             if (h2 == 0) gtm[r * HROW + kt] = gtw;
.LBB0_848:
.LBB0_849:
	v_cmp_gt_i32_e32 vcc, v16, v222
	v_cmp_gt_i32_e64 s[98:99], v1, v222
	v_cmp_gt_i32_e64 s[100:101], v2, v222
	v_cndmask_b32_e64 v15, 0, 2, vcc
	v_cmp_gt_i32_e32 vcc, v3, v222
	v_cndmask_b32_e64 v1, 0, 4, s[98:99]
	v_cmp_gt_i32_e64 s[98:99], v4, v222
	v_cndmask_b32_e64 v2, 0, 8, s[100:101]
	v_cmp_gt_i32_e64 s[100:101], v5, v222
	v_cndmask_b32_e64 v3, 0, v186, vcc
	v_cmp_gt_i32_e32 vcc, v6, v222
	v_cndmask_b32_e64 v4, 0, v193, s[98:99]
	v_cmp_gt_i32_e64 s[98:99], v7, v222
	v_cndmask_b32_e64 v5, 0, v194, s[100:101]
	v_cmp_gt_i32_e64 s[100:101], v8, v222
	v_cndmask_b32_e64 v6, 0, v195, vcc
	v_cmp_gt_i32_e32 vcc, v9, v222
	v_cndmask_b32_e64 v7, 0, v196, s[98:99]
	v_cmp_gt_i32_e64 s[98:99], v10, v222
	v_cndmask_b32_e64 v8, 0, v197, s[100:101]
	v_cmp_gt_i32_e64 s[100:101], v11, v222
	v_cndmask_b32_e64 v9, 0, v198, vcc
	v_cmp_gt_i32_e32 vcc, v12, v222
	v_cndmask_b32_e64 v10, 0, v199, s[98:99]
	v_cmp_gt_i32_e64 s[98:99], v13, v222
	v_cndmask_b32_e64 v11, 0, v200, s[100:101]
	v_cmp_gt_i32_e64 s[100:101], v14, v222
	v_cndmask_b32_e64 v12, 0, v201, vcc
	v_cmp_gt_i32_e32 vcc, v0, v222
	v_cndmask_b32_e64 v13, 0, v202, s[98:99]
	v_cndmask_b32_e64 v14, 0, v203, s[100:101]
	v_cndmask_b32_e64 v0, 0, 1, vcc
	v_or_b32_e32 v0, v15, v0
	v_or3_b32 v0, v0, v1, v2
	v_or3_b32 v0, v0, v3, v4
	v_or3_b32 v0, v0, v5, v6
	v_or3_b32 v0, v0, v7, v8
	v_or3_b32 v0, v0, v9, v10
	v_or3_b32 v0, v0, v11, v12
	v_or3_b32 v0, v0, v13, v14
	v_lshlrev_b32_e32 v0, v219, v0
	v_mov_b32_e32 v1, v0
	s_nop 1
	v_permlane32_swap_b32_e32 v0, v1
	s_and_saveexec_b64 s[6:7], s[84:85]
	v_or_b32_e32 v0, v0, v1
	v_lshl_add_u32 v1, s0, 2, v217
	ds_write_b32 v1, v0 offset:32
	s_or_b64 exec, exec, s[6:7]
	s_mov_b64 s[6:7], -1
	s_branch .LBB0_854

; template <int PH>
; __global__ void __launch_bounds__(NTHR, 2) mk_phase(Args a) { mk_body<PH>(a); }
	.amdhsa_kernel _Z8mk_phaseILin1EEv4Args
		.amdhsa_group_segment_fixed_size 0
		.amdhsa_private_segment_fixed_size 0
		.amdhsa_kernarg_size 456
		.amdhsa_user_sgpr_count 2
		.amdhsa_user_sgpr_dispatch_ptr 0
		.amdhsa_user_sgpr_queue_ptr 0
		.amdhsa_user_sgpr_kernarg_segment_ptr 1
		.amdhsa_user_sgpr_dispatch_id 0
		.amdhsa_user_sgpr_kernarg_preload_length 0
		.amdhsa_user_sgpr_kernarg_preload_offset 0
		.amdhsa_user_sgpr_private_segment_size 0
		.amdhsa_uses_dynamic_stack 0
		.amdhsa_enable_private_segment 0
		.amdhsa_system_sgpr_workgroup_id_x 1
		.amdhsa_system_sgpr_workgroup_id_y 0
		.amdhsa_system_sgpr_workgroup_id_z 0
		.amdhsa_system_sgpr_workgroup_info 0
		.amdhsa_system_vgpr_workitem_id 0
		.amdhsa_next_free_vgpr 255
		.amdhsa_next_free_sgpr 102
		.amdhsa_accum_offset 256
		.amdhsa_reserve_vcc 1
		.amdhsa_float_round_mode_32 0
		.amdhsa_float_round_mode_16_64 0
		.amdhsa_float_denorm_mode_32 3
		.amdhsa_float_denorm_mode_16_64 3
		.amdhsa_dx10_clamp 1
		.amdhsa_ieee_mode 1
		.amdhsa_fp16_overflow 0
		.amdhsa_tg_split 0
		.amdhsa_exception_fp_ieee_invalid_op 0
		.amdhsa_exception_fp_denorm_src 0
		.amdhsa_exception_fp_ieee_div_zero 0
		.amdhsa_exception_fp_ieee_overflow 0
		.amdhsa_exception_fp_ieee_underflow 0
		.amdhsa_exception_fp_ieee_inexact 0
		.amdhsa_exception_int_div_zero 0
	.end_amdhsa_kernel

; template <int PH>
; __global__ void __launch_bounds__(NTHR, 2) mk_phase(Args a) { mk_body<PH>(a); }
.Lfunc_end0:
	.size	_Z8mk_phaseILin1EEv4Args, .Lfunc_end0-_Z8mk_phaseILin1EEv4Args
	.set _Z8mk_phaseILin1EEv4Args.num_vgpr, 255
	.set _Z8mk_phaseILin1EEv4Args.num_agpr, 0
	.set _Z8mk_phaseILin1EEv4Args.numbered_sgpr, 102
	.set _Z8mk_phaseILin1EEv4Args.num_named_barrier, 0
	.set _Z8mk_phaseILin1EEv4Args.private_seg_size, 0
	.set _Z8mk_phaseILin1EEv4Args.uses_vcc, 1
	.set _Z8mk_phaseILin1EEv4Args.uses_flat_scratch, 0
	.set _Z8mk_phaseILin1EEv4Args.has_dyn_sized_stack, 0
	.set _Z8mk_phaseILin1EEv4Args.has_recursion, 0
	.set _Z8mk_phaseILin1EEv4Args.has_indirect_call, 0

; template <int PH>
; __global__ void __launch_bounds__(NTHR, 2) mk_phase(Args a) { mk_body<PH>(a); }
amdhsa.kernels:
  - .agpr_count:     0
    .args:
      - .offset:         0
        .size:           200
        .value_kind:     by_value
      - .offset:         200
        .size:           4
        .value_kind:     hidden_block_count_x
      - .offset:         204
        .size:           4
        .value_kind:     hidden_block_count_y
      - .offset:         208
        .size:           4
        .value_kind:     hidden_block_count_z
      - .offset:         212
        .size:           2
        .value_kind:     hidden_group_size_x
      - .offset:         214
        .size:           2
        .value_kind:     hidden_group_size_y
      - .offset:         216
        .size:           2
        .value_kind:     hidden_group_size_z
      - .offset:         218
        .size:           2
        .value_kind:     hidden_remainder_x
      - .offset:         220
        .size:           2
        .value_kind:     hidden_remainder_y
      - .offset:         222
        .size:           2
        .value_kind:     hidden_remainder_z
      - .offset:         240
        .size:           8
        .value_kind:     hidden_global_offset_x
      - .offset:         248
        .size:           8
        .value_kind:     hidden_global_offset_y
      - .offset:         256
        .size:           8
        .value_kind:     hidden_global_offset_z
      - .offset:         264
        .size:           2
        .value_kind:     hidden_grid_dims
      - .offset:         320
        .size:           4
        .value_kind:     hidden_dynamic_lds_size
    .group_segment_fixed_size: 0
    .kernarg_segment_align: 8
    .kernarg_segment_size: 456
    .language:       OpenCL C
    .language_version:
      - 2
      - 0
    .max_flat_workgroup_size: 512
    .name:           _Z8mk_phaseILin1EEv4Args
    .private_segment_fixed_size: 0
    .sgpr_count:     108
    .sgpr_spill_count: 91
    .symbol:         _Z8mk_phaseILin1EEv4Args.kd
    .uniform_work_group_size: 1
    .uses_dynamic_stack: false
    .vgpr_count:     255
    .vgpr_spill_count: 0
    .wavefront_size: 64
